# diff attention: waves 4-7 issue the next K/V tile DMA right behind their early barrier (before the softmax)
# baseline (speedup 1.0000x reference)
_Z10hybrid_fwd4Args:
	s_load_dword s64, s[0:1], 0xc8
	s_mov_b32 s65, s2
	s_add_u32 s2, s0, 0xc8
	s_addc_u32 s3, s1, 0
	v_readfirstlane_b32 s10, v0
	v_writelane_b32 v255, s2, 0
	s_mov_b32 s66, s65
	s_mov_b32 s100, s10
	s_mov_b32 s101, 0
	s_nop 0
	v_writelane_b32 v255, s3, 1
	s_waitcnt lgkmcnt(0)
	s_and_b32 s2, s64, 7
	s_cmp_lg_u32 s2, 0
	s_cbranch_scc1 .LBB0_1
	s_getpc_b64 s[98:99]

.LBB0_557:
	ds_read_b64_tr_b16 v[144:145], v177 offset:0
	ds_read_b64_tr_b16 v[146:147], v177 offset:0x1000
	ds_read_b64_tr_b16 v[148:149], v177 offset:0x2000
	ds_read_b64_tr_b16 v[150:151], v177 offset:0x3000
	ds_read_b64_tr_b16 v[152:153], v177 offset:0x4000
	ds_read_b64_tr_b16 v[154:155], v177 offset:0x5000
	ds_read_b64_tr_b16 v[156:157], v177 offset:0x6000
	ds_read_b64_tr_b16 v[158:159], v177 offset:0x7000
	ds_read_b64_tr_b16 v[192:193], v177 offset:0x200
	ds_read_b64_tr_b16 v[194:195], v177 offset:0x1200
	ds_read_b64_tr_b16 v[196:197], v177 offset:0x2200
	ds_read_b64_tr_b16 v[198:199], v177 offset:0x3200
	ds_read_b64_tr_b16 v[200:201], v177 offset:0x4200
	ds_read_b64_tr_b16 v[202:203], v177 offset:0x5200
	ds_read_b64_tr_b16 v[204:205], v177 offset:0x6200
	ds_read_b64_tr_b16 v[206:207], v177 offset:0x7200
	s_waitcnt lgkmcnt(8)
	s_nop 0
	v_mfma_f32_32x32x16_bf16 v[112:127], v[144:147], v[128:131], v[112:127]
	v_mfma_f32_32x32x16_bf16 v[112:127], v[148:151], v[132:135], v[112:127]
	v_mfma_f32_32x32x16_bf16 v[112:127], v[152:155], v[136:139], v[112:127]
	v_mfma_f32_32x32x16_bf16 v[112:127], v[156:159], v[140:143], v[112:127]
	ds_read_b64_tr_b16 v[144:145], v177 offset:0x400
	ds_read_b64_tr_b16 v[146:147], v177 offset:0x1400
	ds_read_b64_tr_b16 v[148:149], v177 offset:0x2400
	ds_read_b64_tr_b16 v[150:151], v177 offset:0x3400
	ds_read_b64_tr_b16 v[152:153], v177 offset:0x4400
	ds_read_b64_tr_b16 v[154:155], v177 offset:0x5400
	ds_read_b64_tr_b16 v[156:157], v177 offset:0x6400
	ds_read_b64_tr_b16 v[158:159], v177 offset:0x7400
	s_waitcnt lgkmcnt(8)
	v_mfma_f32_32x32x16_bf16 v[80:95], v[192:195], v[128:131], v[80:95]
	v_mfma_f32_32x32x16_bf16 v[80:95], v[196:199], v[132:135], v[80:95]
	v_mfma_f32_32x32x16_bf16 v[80:95], v[200:203], v[136:139], v[80:95]
	v_mfma_f32_32x32x16_bf16 v[80:95], v[204:207], v[140:143], v[80:95]
	ds_read_b64_tr_b16 v[192:193], v177 offset:0x600
	ds_read_b64_tr_b16 v[194:195], v177 offset:0x1600
	ds_read_b64_tr_b16 v[196:197], v177 offset:0x2600
	ds_read_b64_tr_b16 v[198:199], v177 offset:0x3600
	ds_read_b64_tr_b16 v[200:201], v177 offset:0x4600
	ds_read_b64_tr_b16 v[202:203], v177 offset:0x5600
	ds_read_b64_tr_b16 v[204:205], v177 offset:0x6600
	ds_read_b64_tr_b16 v[206:207], v177 offset:0x7600
	s_waitcnt lgkmcnt(8)
	v_mfma_f32_32x32x16_bf16 v[96:111], v[144:147], v[128:131], v[96:111]
	v_mfma_f32_32x32x16_bf16 v[96:111], v[148:151], v[132:135], v[96:111]
	v_mfma_f32_32x32x16_bf16 v[96:111], v[152:155], v[136:139], v[96:111]
	v_mfma_f32_32x32x16_bf16 v[96:111], v[156:159], v[140:143], v[96:111]
	ds_read_b64_tr_b16 v[144:145], v177 offset:0x800
	ds_read_b64_tr_b16 v[146:147], v177 offset:0x1800
	ds_read_b64_tr_b16 v[148:149], v177 offset:0x2800
	ds_read_b64_tr_b16 v[150:151], v177 offset:0x3800
	ds_read_b64_tr_b16 v[152:153], v177 offset:0x4800
	ds_read_b64_tr_b16 v[154:155], v177 offset:0x5800
	ds_read_b64_tr_b16 v[156:157], v177 offset:0x6800
	ds_read_b64_tr_b16 v[158:159], v177 offset:0x7800
	s_waitcnt lgkmcnt(8)
	v_mfma_f32_32x32x16_bf16 v[64:79], v[192:195], v[128:131], v[64:79]
	v_mfma_f32_32x32x16_bf16 v[64:79], v[196:199], v[132:135], v[64:79]
	v_mfma_f32_32x32x16_bf16 v[64:79], v[200:203], v[136:139], v[64:79]
	v_mfma_f32_32x32x16_bf16 v[64:79], v[204:207], v[140:143], v[64:79]
	ds_read_b64_tr_b16 v[192:193], v177 offset:0xa00
	ds_read_b64_tr_b16 v[194:195], v177 offset:0x1a00
	ds_read_b64_tr_b16 v[196:197], v177 offset:0x2a00
	ds_read_b64_tr_b16 v[198:199], v177 offset:0x3a00
	ds_read_b64_tr_b16 v[200:201], v177 offset:0x4a00
	ds_read_b64_tr_b16 v[202:203], v177 offset:0x5a00
	ds_read_b64_tr_b16 v[204:205], v177 offset:0x6a00
	ds_read_b64_tr_b16 v[206:207], v177 offset:0x7a00
	s_waitcnt lgkmcnt(8)
	v_mfma_f32_32x32x16_bf16 v[48:63], v[144:147], v[128:131], v[48:63]
	v_mfma_f32_32x32x16_bf16 v[48:63], v[148:151], v[132:135], v[48:63]
	v_mfma_f32_32x32x16_bf16 v[48:63], v[152:155], v[136:139], v[48:63]
	v_mfma_f32_32x32x16_bf16 v[48:63], v[156:159], v[140:143], v[48:63]
	ds_read_b64_tr_b16 v[144:145], v177 offset:0xc00
	ds_read_b64_tr_b16 v[146:147], v177 offset:0x1c00
	ds_read_b64_tr_b16 v[148:149], v177 offset:0x2c00
	ds_read_b64_tr_b16 v[150:151], v177 offset:0x3c00
	ds_read_b64_tr_b16 v[152:153], v177 offset:0x4c00
	ds_read_b64_tr_b16 v[154:155], v177 offset:0x5c00
	ds_read_b64_tr_b16 v[156:157], v177 offset:0x6c00
	ds_read_b64_tr_b16 v[158:159], v177 offset:0x7c00
	s_waitcnt lgkmcnt(8)
	v_mfma_f32_32x32x16_bf16 v[32:47], v[192:195], v[128:131], v[32:47]
	v_mfma_f32_32x32x16_bf16 v[32:47], v[196:199], v[132:135], v[32:47]
	v_mfma_f32_32x32x16_bf16 v[32:47], v[200:203], v[136:139], v[32:47]
	v_mfma_f32_32x32x16_bf16 v[32:47], v[204:207], v[140:143], v[32:47]
	ds_read_b64_tr_b16 v[192:193], v177 offset:0xe00
	ds_read_b64_tr_b16 v[194:195], v177 offset:0x1e00
	ds_read_b64_tr_b16 v[196:197], v177 offset:0x2e00
	ds_read_b64_tr_b16 v[198:199], v177 offset:0x3e00
	ds_read_b64_tr_b16 v[200:201], v177 offset:0x4e00
	ds_read_b64_tr_b16 v[202:203], v177 offset:0x5e00
	ds_read_b64_tr_b16 v[204:205], v177 offset:0x6e00
	ds_read_b64_tr_b16 v[206:207], v177 offset:0x7e00
	s_waitcnt lgkmcnt(8)
	v_mfma_f32_32x32x16_bf16 v[16:31], v[144:147], v[128:131], v[16:31]
	v_mfma_f32_32x32x16_bf16 v[16:31], v[148:151], v[132:135], v[16:31]
	v_mfma_f32_32x32x16_bf16 v[16:31], v[152:155], v[136:139], v[16:31]
	v_mfma_f32_32x32x16_bf16 v[16:31], v[156:159], v[140:143], v[16:31]
	s_waitcnt lgkmcnt(0)
	v_mfma_f32_32x32x16_bf16 v[0:15], v[192:195], v[128:131], v[0:15]
	v_mfma_f32_32x32x16_bf16 v[0:15], v[196:199], v[132:135], v[0:15]
	v_mfma_f32_32x32x16_bf16 v[0:15], v[200:203], v[136:139], v[0:15]
	v_mfma_f32_32x32x16_bf16 v[0:15], v[204:207], v[140:143], v[0:15]
	ds_read_b128 v[128:131], v188 offset:0
	ds_read_b128 v[132:135], v188 offset:0x2000
	ds_read_b128 v[136:139], v180 offset:0
	ds_read_b128 v[192:195], v187 offset:0
	ds_read_b128 v[196:199], v187 offset:0x2000
	ds_read_b128 v[200:203], v180 offset:0x400
	s_waitcnt lgkmcnt(3)
	s_nop 0
	v_mfma_f32_32x32x16_bf16 v[144:159], v[128:131], v[136:139], 0
	v_mfma_f32_32x32x16_bf16 v[128:143], v[132:135], v[136:139], 0
	ds_read_b128 v[204:207], v186 offset:0
	ds_read_b128 v[208:211], v186 offset:0x2000
	ds_read_b128 v[212:215], v180 offset:0x800
	s_waitcnt lgkmcnt(3)
	v_mfma_f32_32x32x16_bf16 v[144:159], v[192:195], v[200:203], v[144:159]
	v_mfma_f32_32x32x16_bf16 v[128:143], v[196:199], v[200:203], v[128:143]
	ds_read_b128 v[192:195], v185 offset:0
	ds_read_b128 v[196:199], v185 offset:0x2000
	ds_read_b128 v[200:203], v180 offset:0xc00
	s_waitcnt lgkmcnt(3)
	v_mfma_f32_32x32x16_bf16 v[144:159], v[204:207], v[212:215], v[144:159]
	v_mfma_f32_32x32x16_bf16 v[128:143], v[208:211], v[212:215], v[128:143]
	ds_read_b128 v[204:207], v188 offset:0x80
	ds_read_b128 v[208:211], v188 offset:0x2080
	ds_read_b128 v[212:215], v180 offset:0x1000
	s_waitcnt lgkmcnt(3)
	v_mfma_f32_32x32x16_bf16 v[144:159], v[192:195], v[200:203], v[144:159]
	v_mfma_f32_32x32x16_bf16 v[128:143], v[196:199], v[200:203], v[128:143]
	ds_read_b128 v[192:195], v187 offset:0x80
	ds_read_b128 v[196:199], v187 offset:0x2080
	ds_read_b128 v[200:203], v180 offset:0x1400
	s_waitcnt lgkmcnt(3)
	v_mfma_f32_32x32x16_bf16 v[144:159], v[204:207], v[212:215], v[144:159]
	v_mfma_f32_32x32x16_bf16 v[128:143], v[208:211], v[212:215], v[128:143]
	ds_read_b128 v[204:207], v186 offset:0x80
	ds_read_b128 v[208:211], v186 offset:0x2080
	ds_read_b128 v[212:215], v180 offset:0x1800
	s_waitcnt lgkmcnt(3)
	v_mfma_f32_32x32x16_bf16 v[144:159], v[192:195], v[200:203], v[144:159]
	v_mfma_f32_32x32x16_bf16 v[128:143], v[196:199], v[200:203], v[128:143]
	ds_read_b128 v[192:195], v185 offset:0x80
	ds_read_b128 v[196:199], v185 offset:0x2080
	s_waitcnt lgkmcnt(2)
	v_mfma_f32_32x32x16_bf16 v[144:159], v[204:207], v[212:215], v[144:159]
	v_mfma_f32_32x32x16_bf16 v[128:143], v[208:211], v[212:215], v[128:143]
	s_waitcnt lgkmcnt(0)
	v_mfma_f32_32x32x16_bf16 v[144:159], v[192:195], v[166:169], v[144:159]
	v_mfma_f32_32x32x16_bf16 v[128:143], v[196:199], v[166:169], v[128:143]
	s_bitcmp0_b32 s100, 8
	s_cbranch_scc1 .Lstg_a10
	s_waitcnt vmcnt(0)
	s_waitcnt lgkmcnt(0)
	s_barrier
	s_add_i32 s8, s3, -1
	s_cmp_ge_u32 s8, s75
	s_cbranch_scc1 .Learly_skip_m0_1
	s_add_u32 s6, s66, 0x19f000
	s_addc_u32 s7, s67, 0
	s_mov_b32 m0, s84
	s_nop 0
	global_load_lds_dwordx4 v160, s[6:7]
	s_mov_b32 m0, s85
	s_nop 0
	global_load_lds_dwordx4 v170, s[6:7]
	s_mov_b32 m0, s93
	s_nop 0
	global_load_lds_dwordx4 v162, s[66:67]
	s_add_i32 m0, s2, 0xffffff80
	s_nop 0
	global_load_lds_dwordx4 v162, s[66:67] offset:128
	s_add_i32 m0, s69, 0xffffff00
	s_nop 0
	global_load_lds_dwordx4 v162, s[66:67] offset:256
	s_add_i32 m0, s68, 0xfffffe80
	s_nop 0
	global_load_lds_dwordx4 v162, s[66:67] offset:384
	s_mov_b32 s101, 1
.Learly_skip_m0_1:
.Lstg_a10:
	s_sub_i32 s4, s74, 64
	s_cmp_le_i32 s4, s82
	s_cbranch_scc1 .LBB0_559
	v_add_u32_e32 v172, 64, v189
	v_cmp_gt_i32_e64 s[62:63], 26, v172
	v_cmp_gt_i32_e64 s[64:65], 27, v172
	v_cmp_gt_i32_e64 s[60:61], 25, v172
	s_and_b64 s[62:63], s[64:65], s[62:63]
	v_cmp_gt_i32_e64 s[58:59], 24, v172
	s_and_b64 s[60:61], s[62:63], s[60:61]
	v_cmp_gt_i32_e64 s[56:57], 19, v172
	s_and_b64 s[58:59], s[60:61], s[58:59]
	v_cmp_gt_i32_e64 s[54:55], 18, v172
	s_and_b64 s[56:57], s[58:59], s[56:57]
	v_cmp_gt_i32_e64 s[52:53], 17, v172
	s_and_b64 s[54:55], s[56:57], s[54:55]
	v_cmp_gt_i32_e64 s[50:51], 16, v172
	s_and_b64 s[52:53], s[54:55], s[52:53]
	v_cmp_gt_i32_e64 s[48:49], 11, v172
	s_and_b64 s[50:51], s[52:53], s[50:51]
	v_cmp_gt_i32_e64 s[46:47], 10, v172
	s_and_b64 s[48:49], s[50:51], s[48:49]
	v_cmp_gt_i32_e64 s[44:45], 9, v172
	s_and_b64 s[46:47], s[48:49], s[46:47]
	v_cmp_gt_i32_e64 s[42:43], 8, v172
	s_and_b64 s[44:45], s[46:47], s[44:45]
	v_cmp_gt_i32_e64 s[40:41], 3, v172
	s_and_b64 s[42:43], s[44:45], s[42:43]
	v_cmp_gt_i32_e64 s[38:39], 2, v172
	s_and_b64 s[40:41], s[42:43], s[40:41]
	v_cmp_gt_i32_e64 s[36:37], 1, v172
	s_and_b64 s[38:39], s[40:41], s[38:39]
	v_cmp_gt_i32_e64 s[34:35], 0, v172
	s_and_b64 s[36:37], s[38:39], s[36:37]
	s_and_b64 s[34:35], s[36:37], s[34:35]
	v_cmp_gt_i32_e64 s[30:31], 58, v172
	v_cndmask_b32_e64 v144, v144, v226, s[34:35]
	v_cmp_gt_i32_e64 s[34:35], 59, v172
	v_cmp_gt_i32_e64 s[28:29], 57, v172
	s_and_b64 s[30:31], s[34:35], s[30:31]
	v_cmp_gt_i32_e64 s[26:27], 56, v172
	s_and_b64 s[28:29], s[30:31], s[28:29]
	v_cmp_gt_i32_e64 s[24:25], 51, v172
	s_and_b64 s[26:27], s[28:29], s[26:27]
	v_cmp_gt_i32_e64 s[22:23], 50, v172
	s_and_b64 s[24:25], s[26:27], s[24:25]
	v_cmp_gt_i32_e64 s[20:21], 49, v172
	s_and_b64 s[22:23], s[24:25], s[22:23]
	v_cmp_gt_i32_e64 s[18:19], 48, v172
	s_and_b64 s[20:21], s[22:23], s[20:21]
	v_cmp_gt_i32_e64 s[16:17], 43, v172
	s_and_b64 s[18:19], s[20:21], s[18:19]
	v_cmp_gt_i32_e64 s[14:15], 42, v172
	s_and_b64 s[16:17], s[18:19], s[16:17]
	v_cmp_gt_i32_e64 s[12:13], 41, v172
	s_and_b64 s[14:15], s[16:17], s[14:15]
	v_cmp_gt_i32_e64 s[10:11], 40, v172
	s_and_b64 s[12:13], s[14:15], s[12:13]
	v_cmp_gt_i32_e64 s[8:9], 35, v172
	s_and_b64 s[10:11], s[12:13], s[10:11]
	v_cmp_gt_i32_e64 s[6:7], 34, v172
	s_and_b64 s[8:9], s[10:11], s[8:9]
	v_cmp_gt_i32_e64 s[4:5], 33, v172
	s_and_b64 s[6:7], s[8:9], s[6:7]
	v_cmp_gt_i32_e32 vcc, 32, v172
	s_and_b64 s[4:5], s[6:7], s[4:5]
	s_and_b64 vcc, s[4:5], vcc
	v_cndmask_b32_e64 v159, v159, v226, s[64:65]
	v_cndmask_b32_e64 v158, v158, v226, s[62:63]
	s_mov_b64 s[62:63], 0x100
	v_cndmask_b32_e64 v157, v157, v226, s[60:61]
	v_cndmask_b32_e64 v156, v156, v226, s[58:59]
	v_cndmask_b32_e64 v155, v155, v226, s[56:57]
	v_cndmask_b32_e64 v154, v154, v226, s[54:55]
	v_cndmask_b32_e64 v153, v153, v226, s[52:53]
	v_cndmask_b32_e64 v152, v152, v226, s[50:51]
	v_cndmask_b32_e64 v151, v151, v226, s[48:49]
	v_cndmask_b32_e64 v150, v150, v226, s[46:47]
	v_cndmask_b32_e64 v149, v149, v226, s[44:45]
	v_cndmask_b32_e64 v148, v148, v226, s[42:43]
	v_cndmask_b32_e64 v147, v147, v226, s[40:41]
	v_cndmask_b32_e64 v146, v146, v226, s[38:39]
	v_cndmask_b32_e64 v145, v145, v226, s[36:37]
	v_cndmask_b32_e64 v143, v143, v226, s[34:35]
	v_cndmask_b32_e64 v142, v142, v226, s[30:31]
	v_cndmask_b32_e64 v141, v141, v226, s[28:29]
	v_cndmask_b32_e64 v140, v140, v226, s[26:27]
	v_cndmask_b32_e64 v139, v139, v226, s[24:25]
	v_cndmask_b32_e64 v138, v138, v226, s[22:23]
	v_cndmask_b32_e64 v137, v137, v226, s[20:21]
	v_cndmask_b32_e64 v136, v136, v226, s[18:19]
	v_cndmask_b32_e64 v135, v135, v226, s[16:17]
	v_cndmask_b32_e64 v134, v134, v226, s[14:15]
	v_cndmask_b32_e64 v133, v133, v226, s[12:13]
	v_cndmask_b32_e64 v132, v132, v226, s[10:11]
	v_cndmask_b32_e64 v131, v131, v226, s[8:9]
	v_cndmask_b32_e64 v130, v130, v226, s[6:7]
	v_cndmask_b32_e64 v129, v129, v226, s[4:5]
	v_cndmask_b32_e32 v128, v128, v226, vcc

.LBB0_561:
	s_andn2_b64 vcc, exec, s[6:7]
	s_cbranch_vccnz .LBB0_563
	s_cmp_eq_u32 s101, 1
	s_cbranch_scc1 .LBB0_563
	s_add_u32 s6, s66, 0x19f000
	s_addc_u32 s7, s67, 0
	s_mov_b32 m0, s84
	s_nop 0
	global_load_lds_dwordx4 v160, s[6:7]
	s_mov_b32 m0, s85
	s_nop 0
	global_load_lds_dwordx4 v170, s[6:7]
.LBB0_563:
	v_sub_f32_e32 v144, v190, v172
	v_mul_f32_e32 v144, 0x3e0293ee, v144
	v_exp_f32_e32 v144, v144
	s_nop 0
	v_cndmask_b32_e64 v172, v144, 1.0, s[4:5]
	s_cmp_eq_u32 s101, 1
	s_cbranch_scc1 .Learly_vdone_m0_1
	s_mov_b32 m0, s93
	s_nop 0
	global_load_lds_dwordx4 v162, s[66:67]
	s_add_i32 m0, s2, 0xffffff80
	s_nop 0
	global_load_lds_dwordx4 v162, s[66:67] offset:128
	s_add_i32 m0, s69, 0xffffff00
	s_nop 0
	global_load_lds_dwordx4 v162, s[66:67] offset:256
	s_add_i32 m0, s68, 0xfffffe80
	s_nop 0
	global_load_lds_dwordx4 v162, s[66:67] offset:384
.Learly_vdone_m0_1:
	s_mov_b32 s101, 0
	v_cmp_gt_f32_e32 vcc, 1.0, v172
	s_cbranch_vccz .LBB0_565
	v_pk_mul_f32 v[126:127], v[126:127], v[172:173] op_sel_hi:[1,0]
	v_pk_mul_f32 v[124:125], v[124:125], v[172:173] op_sel_hi:[1,0]
	v_pk_mul_f32 v[122:123], v[122:123], v[172:173] op_sel_hi:[1,0]
	v_pk_mul_f32 v[120:121], v[120:121], v[172:173] op_sel_hi:[1,0]
	v_pk_mul_f32 v[118:119], v[118:119], v[172:173] op_sel_hi:[1,0]
	v_pk_mul_f32 v[116:117], v[116:117], v[172:173] op_sel_hi:[1,0]
	v_pk_mul_f32 v[114:115], v[114:115], v[172:173] op_sel_hi:[1,0]
	v_pk_mul_f32 v[112:113], v[112:113], v[172:173] op_sel_hi:[1,0]
	v_pk_mul_f32 v[94:95], v[94:95], v[172:173] op_sel_hi:[1,0]
	v_pk_mul_f32 v[92:93], v[92:93], v[172:173] op_sel_hi:[1,0]
	v_pk_mul_f32 v[90:91], v[90:91], v[172:173] op_sel_hi:[1,0]
	v_pk_mul_f32 v[88:89], v[88:89], v[172:173] op_sel_hi:[1,0]
	v_pk_mul_f32 v[86:87], v[86:87], v[172:173] op_sel_hi:[1,0]
	v_pk_mul_f32 v[84:85], v[84:85], v[172:173] op_sel_hi:[1,0]
	v_pk_mul_f32 v[82:83], v[82:83], v[172:173] op_sel_hi:[1,0]
	v_pk_mul_f32 v[80:81], v[80:81], v[172:173] op_sel_hi:[1,0]
	v_pk_mul_f32 v[110:111], v[110:111], v[172:173] op_sel_hi:[1,0]
	v_pk_mul_f32 v[108:109], v[108:109], v[172:173] op_sel_hi:[1,0]
	v_pk_mul_f32 v[106:107], v[106:107], v[172:173] op_sel_hi:[1,0]
	v_pk_mul_f32 v[104:105], v[104:105], v[172:173] op_sel_hi:[1,0]
	v_pk_mul_f32 v[102:103], v[102:103], v[172:173] op_sel_hi:[1,0]
	v_pk_mul_f32 v[100:101], v[100:101], v[172:173] op_sel_hi:[1,0]
	v_pk_mul_f32 v[98:99], v[98:99], v[172:173] op_sel_hi:[1,0]
	v_pk_mul_f32 v[96:97], v[96:97], v[172:173] op_sel_hi:[1,0]
	v_pk_mul_f32 v[78:79], v[78:79], v[172:173] op_sel_hi:[1,0]
	v_pk_mul_f32 v[76:77], v[76:77], v[172:173] op_sel_hi:[1,0]
	v_pk_mul_f32 v[74:75], v[74:75], v[172:173] op_sel_hi:[1,0]
	v_pk_mul_f32 v[72:73], v[72:73], v[172:173] op_sel_hi:[1,0]
	v_pk_mul_f32 v[70:71], v[70:71], v[172:173] op_sel_hi:[1,0]
	v_pk_mul_f32 v[68:69], v[68:69], v[172:173] op_sel_hi:[1,0]
	v_pk_mul_f32 v[66:67], v[66:67], v[172:173] op_sel_hi:[1,0]
	v_pk_mul_f32 v[64:65], v[64:65], v[172:173] op_sel_hi:[1,0]
	v_pk_mul_f32 v[62:63], v[62:63], v[172:173] op_sel_hi:[1,0]
	v_pk_mul_f32 v[60:61], v[60:61], v[172:173] op_sel_hi:[1,0]
	v_pk_mul_f32 v[58:59], v[58:59], v[172:173] op_sel_hi:[1,0]
	v_pk_mul_f32 v[56:57], v[56:57], v[172:173] op_sel_hi:[1,0]
	v_pk_mul_f32 v[54:55], v[54:55], v[172:173] op_sel_hi:[1,0]
	v_pk_mul_f32 v[52:53], v[52:53], v[172:173] op_sel_hi:[1,0]
	v_pk_mul_f32 v[50:51], v[50:51], v[172:173] op_sel_hi:[1,0]
	v_pk_mul_f32 v[48:49], v[48:49], v[172:173] op_sel_hi:[1,0]
	v_pk_mul_f32 v[46:47], v[46:47], v[172:173] op_sel_hi:[1,0]
	v_pk_mul_f32 v[44:45], v[44:45], v[172:173] op_sel_hi:[1,0]
	v_pk_mul_f32 v[42:43], v[42:43], v[172:173] op_sel_hi:[1,0]
	v_pk_mul_f32 v[40:41], v[40:41], v[172:173] op_sel_hi:[1,0]
	v_pk_mul_f32 v[38:39], v[38:39], v[172:173] op_sel_hi:[1,0]
	v_pk_mul_f32 v[36:37], v[36:37], v[172:173] op_sel_hi:[1,0]
	v_pk_mul_f32 v[34:35], v[34:35], v[172:173] op_sel_hi:[1,0]
	v_pk_mul_f32 v[32:33], v[32:33], v[172:173] op_sel_hi:[1,0]
	v_pk_mul_f32 v[30:31], v[30:31], v[172:173] op_sel_hi:[1,0]
	v_pk_mul_f32 v[28:29], v[28:29], v[172:173] op_sel_hi:[1,0]
	v_pk_mul_f32 v[26:27], v[26:27], v[172:173] op_sel_hi:[1,0]
	v_pk_mul_f32 v[24:25], v[24:25], v[172:173] op_sel_hi:[1,0]
	v_pk_mul_f32 v[22:23], v[22:23], v[172:173] op_sel_hi:[1,0]
	v_pk_mul_f32 v[20:21], v[20:21], v[172:173] op_sel_hi:[1,0]
	v_pk_mul_f32 v[18:19], v[18:19], v[172:173] op_sel_hi:[1,0]
	v_pk_mul_f32 v[16:17], v[16:17], v[172:173] op_sel_hi:[1,0]
	v_pk_mul_f32 v[14:15], v[14:15], v[172:173] op_sel_hi:[1,0]
	v_pk_mul_f32 v[12:13], v[12:13], v[172:173] op_sel_hi:[1,0]
	v_pk_mul_f32 v[10:11], v[10:11], v[172:173] op_sel_hi:[1,0]
	v_pk_mul_f32 v[8:9], v[8:9], v[172:173] op_sel_hi:[1,0]
	v_pk_mul_f32 v[6:7], v[6:7], v[172:173] op_sel_hi:[1,0]
	v_pk_mul_f32 v[4:5], v[4:5], v[172:173] op_sel_hi:[1,0]
	v_pk_mul_f32 v[2:3], v[2:3], v[172:173] op_sel_hi:[1,0]
	v_pk_mul_f32 v[0:1], v[0:1], v[172:173] op_sel_hi:[1,0]
.LBB0_565:
	ds_read_b64_tr_b16 v[144:145], v177 offset:0x8000
	ds_read_b64_tr_b16 v[146:147], v177 offset:0x9000
	ds_read_b64_tr_b16 v[148:149], v177 offset:0xa000
	ds_read_b64_tr_b16 v[150:151], v177 offset:0xb000
	ds_read_b64_tr_b16 v[152:153], v177 offset:0xc000
	ds_read_b64_tr_b16 v[154:155], v177 offset:0xd000
	ds_read_b64_tr_b16 v[156:157], v177 offset:0xe000
	ds_read_b64_tr_b16 v[158:159], v177 offset:0xf000
	ds_read_b64_tr_b16 v[194:195], v177 offset:0x8200
	ds_read_b64_tr_b16 v[196:197], v177 offset:0x9200
	ds_read_b64_tr_b16 v[198:199], v177 offset:0xa200
	ds_read_b64_tr_b16 v[200:201], v177 offset:0xb200
	ds_read_b64_tr_b16 v[202:203], v177 offset:0xc200
	ds_read_b64_tr_b16 v[204:205], v177 offset:0xd200
	ds_read_b64_tr_b16 v[206:207], v177 offset:0xe200
	ds_read_b64_tr_b16 v[208:209], v177 offset:0xf200
	s_waitcnt lgkmcnt(8)
	s_nop 0
	v_mfma_f32_32x32x16_bf16 v[112:127], v[144:147], v[128:131], v[112:127]
	v_mfma_f32_32x32x16_bf16 v[112:127], v[148:151], v[132:135], v[112:127]
	v_mfma_f32_32x32x16_bf16 v[112:127], v[152:155], v[136:139], v[112:127]
	v_mfma_f32_32x32x16_bf16 v[112:127], v[156:159], v[140:143], v[112:127]
	ds_read_b64_tr_b16 v[144:145], v177 offset:0x8400
	ds_read_b64_tr_b16 v[146:147], v177 offset:0x9400
	ds_read_b64_tr_b16 v[148:149], v177 offset:0xa400
	ds_read_b64_tr_b16 v[150:151], v177 offset:0xb400
	ds_read_b64_tr_b16 v[152:153], v177 offset:0xc400
	ds_read_b64_tr_b16 v[154:155], v177 offset:0xd400
	ds_read_b64_tr_b16 v[156:157], v177 offset:0xe400
	ds_read_b64_tr_b16 v[158:159], v177 offset:0xf400
	s_waitcnt lgkmcnt(8)
	v_mfma_f32_32x32x16_bf16 v[80:95], v[194:197], v[128:131], v[80:95]
	v_mfma_f32_32x32x16_bf16 v[80:95], v[198:201], v[132:135], v[80:95]
	v_mfma_f32_32x32x16_bf16 v[80:95], v[202:205], v[136:139], v[80:95]
	v_mfma_f32_32x32x16_bf16 v[80:95], v[206:209], v[140:143], v[80:95]
	ds_read_b64_tr_b16 v[194:195], v177 offset:0x8600
	ds_read_b64_tr_b16 v[196:197], v177 offset:0x9600
	ds_read_b64_tr_b16 v[198:199], v177 offset:0xa600
	ds_read_b64_tr_b16 v[200:201], v177 offset:0xb600
	ds_read_b64_tr_b16 v[202:203], v177 offset:0xc600
	ds_read_b64_tr_b16 v[204:205], v177 offset:0xd600
	ds_read_b64_tr_b16 v[206:207], v177 offset:0xe600
	ds_read_b64_tr_b16 v[208:209], v177 offset:0xf600
	s_waitcnt lgkmcnt(8)
	v_mfma_f32_32x32x16_bf16 v[96:111], v[144:147], v[128:131], v[96:111]
	v_mfma_f32_32x32x16_bf16 v[96:111], v[148:151], v[132:135], v[96:111]
	v_mfma_f32_32x32x16_bf16 v[96:111], v[152:155], v[136:139], v[96:111]
	v_mfma_f32_32x32x16_bf16 v[96:111], v[156:159], v[140:143], v[96:111]
	ds_read_b64_tr_b16 v[144:145], v177 offset:0x8800
	ds_read_b64_tr_b16 v[146:147], v177 offset:0x9800
	ds_read_b64_tr_b16 v[148:149], v177 offset:0xa800
	ds_read_b64_tr_b16 v[150:151], v177 offset:0xb800
	ds_read_b64_tr_b16 v[152:153], v177 offset:0xc800
	ds_read_b64_tr_b16 v[154:155], v177 offset:0xd800
	ds_read_b64_tr_b16 v[156:157], v177 offset:0xe800
	ds_read_b64_tr_b16 v[158:159], v177 offset:0xf800
	s_waitcnt lgkmcnt(8)
	v_mfma_f32_32x32x16_bf16 v[64:79], v[194:197], v[128:131], v[64:79]
	v_mfma_f32_32x32x16_bf16 v[64:79], v[198:201], v[132:135], v[64:79]
	v_mfma_f32_32x32x16_bf16 v[64:79], v[202:205], v[136:139], v[64:79]
	v_mfma_f32_32x32x16_bf16 v[64:79], v[206:209], v[140:143], v[64:79]
	ds_read_b64_tr_b16 v[194:195], v177 offset:0x8a00
	ds_read_b64_tr_b16 v[196:197], v177 offset:0x9a00
	ds_read_b64_tr_b16 v[198:199], v177 offset:0xaa00
	ds_read_b64_tr_b16 v[200:201], v177 offset:0xba00
	ds_read_b64_tr_b16 v[202:203], v177 offset:0xca00
	ds_read_b64_tr_b16 v[204:205], v177 offset:0xda00
	ds_read_b64_tr_b16 v[206:207], v177 offset:0xea00
	ds_read_b64_tr_b16 v[208:209], v177 offset:0xfa00
	s_waitcnt lgkmcnt(8)
	v_mfma_f32_32x32x16_bf16 v[48:63], v[144:147], v[128:131], v[48:63]
	v_mfma_f32_32x32x16_bf16 v[48:63], v[148:151], v[132:135], v[48:63]
	v_mfma_f32_32x32x16_bf16 v[48:63], v[152:155], v[136:139], v[48:63]
	v_mfma_f32_32x32x16_bf16 v[48:63], v[156:159], v[140:143], v[48:63]
	ds_read_b64_tr_b16 v[144:145], v177 offset:0x8c00
	ds_read_b64_tr_b16 v[146:147], v177 offset:0x9c00
	ds_read_b64_tr_b16 v[148:149], v177 offset:0xac00
	ds_read_b64_tr_b16 v[150:151], v177 offset:0xbc00
	ds_read_b64_tr_b16 v[152:153], v177 offset:0xcc00
	ds_read_b64_tr_b16 v[154:155], v177 offset:0xdc00
	ds_read_b64_tr_b16 v[156:157], v177 offset:0xec00
	ds_read_b64_tr_b16 v[158:159], v177 offset:0xfc00
	s_waitcnt lgkmcnt(8)
	v_mfma_f32_32x32x16_bf16 v[32:47], v[194:197], v[128:131], v[32:47]
	v_mfma_f32_32x32x16_bf16 v[32:47], v[198:201], v[132:135], v[32:47]
	v_mfma_f32_32x32x16_bf16 v[32:47], v[202:205], v[136:139], v[32:47]
	v_mfma_f32_32x32x16_bf16 v[32:47], v[206:209], v[140:143], v[32:47]
	ds_read_b64_tr_b16 v[194:195], v177 offset:0x8e00
	ds_read_b64_tr_b16 v[196:197], v177 offset:0x9e00
	ds_read_b64_tr_b16 v[198:199], v177 offset:0xae00
	ds_read_b64_tr_b16 v[200:201], v177 offset:0xbe00
	ds_read_b64_tr_b16 v[202:203], v177 offset:0xce00
	ds_read_b64_tr_b16 v[204:205], v177 offset:0xde00
	ds_read_b64_tr_b16 v[206:207], v177 offset:0xee00
	ds_read_b64_tr_b16 v[208:209], v177 offset:0xfe00
	s_waitcnt lgkmcnt(8)
	v_mfma_f32_32x32x16_bf16 v[16:31], v[144:147], v[128:131], v[16:31]
	v_mfma_f32_32x32x16_bf16 v[16:31], v[148:151], v[132:135], v[16:31]
	v_mfma_f32_32x32x16_bf16 v[16:31], v[152:155], v[136:139], v[16:31]
	v_mfma_f32_32x32x16_bf16 v[16:31], v[156:159], v[140:143], v[16:31]
	s_waitcnt lgkmcnt(0)
	v_mfma_f32_32x32x16_bf16 v[0:15], v[194:197], v[128:131], v[0:15]
	v_mfma_f32_32x32x16_bf16 v[0:15], v[198:201], v[132:135], v[0:15]
	v_mfma_f32_32x32x16_bf16 v[0:15], v[202:205], v[136:139], v[0:15]
	v_mfma_f32_32x32x16_bf16 v[0:15], v[206:209], v[140:143], v[0:15]
	ds_read_b128 v[128:131], v181 offset:0
	ds_read_b128 v[132:135], v181 offset:0x2000
	ds_read_b128 v[136:139], v180 offset:0
	ds_read_b128 v[194:197], v182 offset:0
	ds_read_b128 v[198:201], v182 offset:0x2000
	ds_read_b128 v[202:205], v180 offset:0x400
	s_waitcnt lgkmcnt(3)
	s_nop 0
	v_mfma_f32_32x32x16_bf16 v[144:159], v[128:131], v[136:139], 0
	v_mfma_f32_32x32x16_bf16 v[128:143], v[132:135], v[136:139], 0
	ds_read_b128 v[206:209], v183 offset:0
	ds_read_b128 v[210:213], v183 offset:0x2000
	ds_read_b128 v[214:217], v180 offset:0x800
	s_waitcnt lgkmcnt(3)
	v_mfma_f32_32x32x16_bf16 v[144:159], v[194:197], v[202:205], v[144:159]
	v_mfma_f32_32x32x16_bf16 v[128:143], v[198:201], v[202:205], v[128:143]
	ds_read_b128 v[194:197], v184 offset:0
	ds_read_b128 v[198:201], v184 offset:0x2000
	ds_read_b128 v[202:205], v180 offset:0xc00
	s_waitcnt lgkmcnt(3)
	v_mfma_f32_32x32x16_bf16 v[144:159], v[206:209], v[214:217], v[144:159]
	v_mfma_f32_32x32x16_bf16 v[128:143], v[210:213], v[214:217], v[128:143]
	ds_read_b128 v[206:209], v181 offset:0x80
	ds_read_b128 v[210:213], v181 offset:0x2080
	ds_read_b128 v[214:217], v180 offset:0x1000
	s_waitcnt lgkmcnt(3)
	v_mfma_f32_32x32x16_bf16 v[144:159], v[194:197], v[202:205], v[144:159]
	v_mfma_f32_32x32x16_bf16 v[128:143], v[198:201], v[202:205], v[128:143]
	ds_read_b128 v[194:197], v182 offset:0x80
	ds_read_b128 v[198:201], v182 offset:0x2080
	ds_read_b128 v[202:205], v180 offset:0x1400
	s_waitcnt lgkmcnt(3)
	v_mfma_f32_32x32x16_bf16 v[144:159], v[206:209], v[214:217], v[144:159]
	v_mfma_f32_32x32x16_bf16 v[128:143], v[210:213], v[214:217], v[128:143]
	ds_read_b128 v[206:209], v183 offset:0x80
	ds_read_b128 v[210:213], v183 offset:0x2080
	ds_read_b128 v[214:217], v180 offset:0x1800
	s_waitcnt lgkmcnt(3)
	v_mfma_f32_32x32x16_bf16 v[144:159], v[194:197], v[202:205], v[144:159]
	v_mfma_f32_32x32x16_bf16 v[128:143], v[198:201], v[202:205], v[128:143]
	ds_read_b128 v[194:197], v184 offset:0x80
	ds_read_b128 v[198:201], v184 offset:0x2080
	s_waitcnt lgkmcnt(2)
	v_mfma_f32_32x32x16_bf16 v[144:159], v[206:209], v[214:217], v[144:159]
	v_mfma_f32_32x32x16_bf16 v[128:143], v[210:213], v[214:217], v[128:143]
	s_waitcnt lgkmcnt(0)
	v_mfma_f32_32x32x16_bf16 v[144:159], v[194:197], v[166:169], v[144:159]
	v_mfma_f32_32x32x16_bf16 v[128:143], v[198:201], v[166:169], v[128:143]
	s_bitcmp0_b32 s100, 8
	s_cbranch_scc1 .Lstg_a11
	s_waitcnt vmcnt(0)
	s_waitcnt lgkmcnt(0)
	s_barrier
	s_cmp_lt_u32 s3, s75
	s_cbranch_scc0 .Learly_skip_m0_2
	s_add_u32 s6, s66, 0x33f000
	s_addc_u32 s7, s67, 0
	s_mov_b32 m0, s83
	s_nop 0
	global_load_lds_dwordx4 v160, s[6:7]
	s_mov_b32 m0, s78
	s_nop 0
	global_load_lds_dwordx4 v170, s[6:7]
	s_add_u32 s6, s66, 0x1a0000
	s_addc_u32 s7, s67, 0
	s_mov_b32 m0, s90
	s_nop 0
	global_load_lds_dwordx4 v162, s[6:7]
	s_add_i32 m0, s91, 0xffffff80
	s_nop 0
	global_load_lds_dwordx4 v162, s[6:7] offset:128
	s_add_i32 m0, s88, 0xffffff00
	s_nop 0
	global_load_lds_dwordx4 v162, s[6:7] offset:256
	s_add_i32 m0, s89, 0xfffffe80
	s_nop 0
	global_load_lds_dwordx4 v162, s[6:7] offset:384
	s_mov_b32 s101, 1
.Learly_skip_m0_2:
.Lstg_a11:
	s_cmp_le_i32 s74, s82
	s_cbranch_scc1 .LBB0_567
	v_cmp_gt_i32_e64 s[62:63], 26, v189
	v_cmp_gt_i32_e64 s[64:65], 27, v189
	v_cmp_gt_i32_e64 s[60:61], 25, v189
	s_and_b64 s[62:63], s[64:65], s[62:63]
	v_cmp_gt_i32_e64 s[58:59], 24, v189
	s_and_b64 s[60:61], s[62:63], s[60:61]
	v_cmp_gt_i32_e64 s[56:57], 19, v189
	s_and_b64 s[58:59], s[60:61], s[58:59]
	v_cmp_gt_i32_e64 s[54:55], 18, v189
	s_and_b64 s[56:57], s[58:59], s[56:57]
	v_cmp_gt_i32_e64 s[52:53], 17, v189
	s_and_b64 s[54:55], s[56:57], s[54:55]
	v_cmp_gt_i32_e64 s[50:51], 16, v189
	s_and_b64 s[52:53], s[54:55], s[52:53]
	v_cmp_gt_i32_e64 s[48:49], 11, v189
	s_and_b64 s[50:51], s[52:53], s[50:51]
	v_cmp_gt_i32_e64 s[46:47], 10, v189
	s_and_b64 s[48:49], s[50:51], s[48:49]
	v_cmp_gt_i32_e64 s[44:45], 9, v189
	s_and_b64 s[46:47], s[48:49], s[46:47]
	v_cmp_gt_i32_e64 s[42:43], 8, v189
	s_and_b64 s[44:45], s[46:47], s[44:45]
	v_cmp_gt_i32_e64 s[40:41], 3, v189
	s_and_b64 s[42:43], s[44:45], s[42:43]
	v_cmp_gt_i32_e64 s[38:39], 2, v189
	s_and_b64 s[40:41], s[42:43], s[40:41]
	v_cmp_gt_i32_e64 s[36:37], 1, v189
	s_and_b64 s[38:39], s[40:41], s[38:39]
	v_cmp_gt_i32_e64 s[34:35], 0, v189
	s_and_b64 s[36:37], s[38:39], s[36:37]
	s_and_b64 s[34:35], s[36:37], s[34:35]
	v_cmp_gt_i32_e64 s[30:31], 58, v189
	v_cndmask_b32_e64 v144, v144, v226, s[34:35]
	v_cmp_gt_i32_e64 s[34:35], 59, v189
	v_cmp_gt_i32_e64 s[28:29], 57, v189
	s_and_b64 s[30:31], s[34:35], s[30:31]
	v_cmp_gt_i32_e64 s[26:27], 56, v189
	s_and_b64 s[28:29], s[30:31], s[28:29]
	v_cmp_gt_i32_e64 s[24:25], 51, v189
	s_and_b64 s[26:27], s[28:29], s[26:27]
	v_cmp_gt_i32_e64 s[22:23], 50, v189
	s_and_b64 s[24:25], s[26:27], s[24:25]
	v_cmp_gt_i32_e64 s[20:21], 49, v189
	s_and_b64 s[22:23], s[24:25], s[22:23]
	v_cmp_gt_i32_e64 s[18:19], 48, v189
	s_and_b64 s[20:21], s[22:23], s[20:21]
	v_cmp_gt_i32_e64 s[16:17], 43, v189
	s_and_b64 s[18:19], s[20:21], s[18:19]
	v_cmp_gt_i32_e64 s[14:15], 42, v189
	s_and_b64 s[16:17], s[18:19], s[16:17]
	v_cmp_gt_i32_e64 s[12:13], 41, v189
	s_and_b64 s[14:15], s[16:17], s[14:15]
	v_cmp_gt_i32_e64 s[10:11], 40, v189
	s_and_b64 s[12:13], s[14:15], s[12:13]
	v_cmp_gt_i32_e64 s[8:9], 35, v189
	s_and_b64 s[10:11], s[12:13], s[10:11]
	v_cmp_gt_i32_e64 s[6:7], 34, v189
	s_and_b64 s[8:9], s[10:11], s[8:9]
	v_cmp_gt_i32_e64 s[4:5], 33, v189
	s_and_b64 s[6:7], s[8:9], s[6:7]
	v_cmp_gt_i32_e32 vcc, 32, v189
	s_and_b64 s[4:5], s[6:7], s[4:5]
	s_and_b64 vcc, s[4:5], vcc
	v_cndmask_b32_e64 v159, v159, v226, s[64:65]
	v_cndmask_b32_e64 v158, v158, v226, s[62:63]
	s_mov_b64 s[62:63], 0x100
	v_cndmask_b32_e64 v157, v157, v226, s[60:61]
	v_cndmask_b32_e64 v156, v156, v226, s[58:59]
	v_cndmask_b32_e64 v155, v155, v226, s[56:57]
	v_cndmask_b32_e64 v154, v154, v226, s[54:55]
	v_cndmask_b32_e64 v153, v153, v226, s[52:53]
	v_cndmask_b32_e64 v152, v152, v226, s[50:51]
	v_cndmask_b32_e64 v151, v151, v226, s[48:49]
	v_cndmask_b32_e64 v150, v150, v226, s[46:47]
	v_cndmask_b32_e64 v149, v149, v226, s[44:45]
	v_cndmask_b32_e64 v148, v148, v226, s[42:43]
	v_cndmask_b32_e64 v147, v147, v226, s[40:41]
	v_cndmask_b32_e64 v146, v146, v226, s[38:39]
	v_cndmask_b32_e64 v145, v145, v226, s[36:37]
	v_cndmask_b32_e64 v143, v143, v226, s[34:35]
	v_cndmask_b32_e64 v142, v142, v226, s[30:31]
	v_cndmask_b32_e64 v141, v141, v226, s[28:29]
	v_cndmask_b32_e64 v140, v140, v226, s[26:27]
	v_cndmask_b32_e64 v139, v139, v226, s[24:25]
	v_cndmask_b32_e64 v138, v138, v226, s[22:23]
	v_cndmask_b32_e64 v137, v137, v226, s[20:21]
	v_cndmask_b32_e64 v136, v136, v226, s[18:19]
	v_cndmask_b32_e64 v135, v135, v226, s[16:17]
	v_cndmask_b32_e64 v134, v134, v226, s[14:15]
	v_cndmask_b32_e64 v133, v133, v226, s[12:13]
	v_cndmask_b32_e64 v132, v132, v226, s[10:11]
	v_cndmask_b32_e64 v131, v131, v226, s[8:9]
	v_cndmask_b32_e64 v130, v130, v226, s[6:7]
	v_cndmask_b32_e64 v129, v129, v226, s[4:5]
	v_cndmask_b32_e32 v128, v128, v226, vcc

.LBB0_570:
	s_andn2_b64 vcc, exec, s[6:7]
	s_cbranch_vccnz .LBB0_572
	s_cmp_eq_u32 s101, 1
	s_cbranch_scc1 .LBB0_572
	s_add_u32 s6, s66, 0x33f000
	s_addc_u32 s7, s67, 0
	s_mov_b32 m0, s83
	s_nop 0
	global_load_lds_dwordx4 v160, s[6:7]
	s_mov_b32 m0, s78
	s_nop 0
	global_load_lds_dwordx4 v170, s[6:7]

.LBB0_574:
	s_andn2_b64 vcc, exec, s[6:7]
	s_cbranch_vccnz .LBB0_576
	s_cmp_eq_u32 s101, 1
	s_cbranch_scc1 .LBB0_576
	s_add_u32 s6, s66, 0x1a0000
	s_addc_u32 s7, s67, 0
	s_mov_b32 m0, s90
	s_nop 0
	global_load_lds_dwordx4 v162, s[6:7]
	s_add_i32 m0, s91, 0xffffff80
	s_nop 0
	global_load_lds_dwordx4 v162, s[6:7] offset:128
	s_add_i32 m0, s88, 0xffffff00
	s_nop 0
	global_load_lds_dwordx4 v162, s[6:7] offset:256
	s_add_i32 m0, s89, 0xfffffe80
	s_nop 0
	global_load_lds_dwordx4 v162, s[6:7] offset:384
.LBB0_576:
	s_mov_b32 s101, 0
	v_sub_f32_e32 v144, v193, v198
	v_mul_f32_e32 v144, 0x3e0293ee, v144
	v_exp_f32_e32 v144, v144
	s_nop 0
	v_cndmask_b32_e64 v144, v144, 1.0, s[4:5]
	v_cmp_gt_f32_e32 vcc, 1.0, v144
	s_cbranch_vccz .LBB0_578
	v_pk_mul_f32 v[126:127], v[126:127], v[144:145] op_sel_hi:[1,0]
	v_pk_mul_f32 v[124:125], v[124:125], v[144:145] op_sel_hi:[1,0]
	v_pk_mul_f32 v[122:123], v[122:123], v[144:145] op_sel_hi:[1,0]
	v_pk_mul_f32 v[120:121], v[120:121], v[144:145] op_sel_hi:[1,0]
	v_pk_mul_f32 v[118:119], v[118:119], v[144:145] op_sel_hi:[1,0]
	v_pk_mul_f32 v[116:117], v[116:117], v[144:145] op_sel_hi:[1,0]
	v_pk_mul_f32 v[114:115], v[114:115], v[144:145] op_sel_hi:[1,0]
	v_pk_mul_f32 v[112:113], v[112:113], v[144:145] op_sel_hi:[1,0]
	v_pk_mul_f32 v[94:95], v[94:95], v[144:145] op_sel_hi:[1,0]
	v_pk_mul_f32 v[92:93], v[92:93], v[144:145] op_sel_hi:[1,0]
	v_pk_mul_f32 v[90:91], v[90:91], v[144:145] op_sel_hi:[1,0]
	v_pk_mul_f32 v[88:89], v[88:89], v[144:145] op_sel_hi:[1,0]
	v_pk_mul_f32 v[86:87], v[86:87], v[144:145] op_sel_hi:[1,0]
	v_pk_mul_f32 v[84:85], v[84:85], v[144:145] op_sel_hi:[1,0]
	v_pk_mul_f32 v[82:83], v[82:83], v[144:145] op_sel_hi:[1,0]
	v_pk_mul_f32 v[80:81], v[80:81], v[144:145] op_sel_hi:[1,0]
	v_pk_mul_f32 v[110:111], v[110:111], v[144:145] op_sel_hi:[1,0]
	v_pk_mul_f32 v[108:109], v[108:109], v[144:145] op_sel_hi:[1,0]
	v_pk_mul_f32 v[106:107], v[106:107], v[144:145] op_sel_hi:[1,0]
	v_pk_mul_f32 v[104:105], v[104:105], v[144:145] op_sel_hi:[1,0]
	v_pk_mul_f32 v[102:103], v[102:103], v[144:145] op_sel_hi:[1,0]
	v_pk_mul_f32 v[100:101], v[100:101], v[144:145] op_sel_hi:[1,0]
	v_pk_mul_f32 v[98:99], v[98:99], v[144:145] op_sel_hi:[1,0]
	v_pk_mul_f32 v[96:97], v[96:97], v[144:145] op_sel_hi:[1,0]
	v_pk_mul_f32 v[78:79], v[78:79], v[144:145] op_sel_hi:[1,0]
	v_pk_mul_f32 v[76:77], v[76:77], v[144:145] op_sel_hi:[1,0]
	v_pk_mul_f32 v[74:75], v[74:75], v[144:145] op_sel_hi:[1,0]
	v_pk_mul_f32 v[72:73], v[72:73], v[144:145] op_sel_hi:[1,0]
	v_pk_mul_f32 v[70:71], v[70:71], v[144:145] op_sel_hi:[1,0]
	v_pk_mul_f32 v[68:69], v[68:69], v[144:145] op_sel_hi:[1,0]
	v_pk_mul_f32 v[66:67], v[66:67], v[144:145] op_sel_hi:[1,0]
	v_pk_mul_f32 v[64:65], v[64:65], v[144:145] op_sel_hi:[1,0]
	v_pk_mul_f32 v[62:63], v[62:63], v[144:145] op_sel_hi:[1,0]
	v_pk_mul_f32 v[60:61], v[60:61], v[144:145] op_sel_hi:[1,0]
	v_pk_mul_f32 v[58:59], v[58:59], v[144:145] op_sel_hi:[1,0]
	v_pk_mul_f32 v[56:57], v[56:57], v[144:145] op_sel_hi:[1,0]
	v_pk_mul_f32 v[54:55], v[54:55], v[144:145] op_sel_hi:[1,0]
	v_pk_mul_f32 v[52:53], v[52:53], v[144:145] op_sel_hi:[1,0]
	v_pk_mul_f32 v[50:51], v[50:51], v[144:145] op_sel_hi:[1,0]
	v_pk_mul_f32 v[48:49], v[48:49], v[144:145] op_sel_hi:[1,0]
	v_pk_mul_f32 v[46:47], v[46:47], v[144:145] op_sel_hi:[1,0]
	v_pk_mul_f32 v[44:45], v[44:45], v[144:145] op_sel_hi:[1,0]
	v_pk_mul_f32 v[42:43], v[42:43], v[144:145] op_sel_hi:[1,0]
	v_pk_mul_f32 v[40:41], v[40:41], v[144:145] op_sel_hi:[1,0]
	v_pk_mul_f32 v[38:39], v[38:39], v[144:145] op_sel_hi:[1,0]
	v_pk_mul_f32 v[36:37], v[36:37], v[144:145] op_sel_hi:[1,0]
	v_pk_mul_f32 v[34:35], v[34:35], v[144:145] op_sel_hi:[1,0]
	v_pk_mul_f32 v[32:33], v[32:33], v[144:145] op_sel_hi:[1,0]
	v_pk_mul_f32 v[30:31], v[30:31], v[144:145] op_sel_hi:[1,0]
	v_pk_mul_f32 v[28:29], v[28:29], v[144:145] op_sel_hi:[1,0]
	v_pk_mul_f32 v[26:27], v[26:27], v[144:145] op_sel_hi:[1,0]
	v_pk_mul_f32 v[24:25], v[24:25], v[144:145] op_sel_hi:[1,0]
	v_pk_mul_f32 v[22:23], v[22:23], v[144:145] op_sel_hi:[1,0]
	v_pk_mul_f32 v[20:21], v[20:21], v[144:145] op_sel_hi:[1,0]
	v_pk_mul_f32 v[18:19], v[18:19], v[144:145] op_sel_hi:[1,0]
	v_pk_mul_f32 v[16:17], v[16:17], v[144:145] op_sel_hi:[1,0]
	v_pk_mul_f32 v[14:15], v[14:15], v[144:145] op_sel_hi:[1,0]
	v_pk_mul_f32 v[12:13], v[12:13], v[144:145] op_sel_hi:[1,0]
	v_pk_mul_f32 v[10:11], v[10:11], v[144:145] op_sel_hi:[1,0]
	v_pk_mul_f32 v[8:9], v[8:9], v[144:145] op_sel_hi:[1,0]
	v_pk_mul_f32 v[6:7], v[6:7], v[144:145] op_sel_hi:[1,0]
	v_pk_mul_f32 v[4:5], v[4:5], v[144:145] op_sel_hi:[1,0]
	v_pk_mul_f32 v[2:3], v[2:3], v[144:145] op_sel_hi:[1,0]
	v_pk_mul_f32 v[0:1], v[0:1], v[144:145] op_sel_hi:[1,0]

.LBB0_589:
	ds_read_b64_tr_b16 v[144:145], v177 offset:0
	ds_read_b64_tr_b16 v[146:147], v177 offset:0x1000
	ds_read_b64_tr_b16 v[148:149], v177 offset:0x2000
	ds_read_b64_tr_b16 v[150:151], v177 offset:0x3000
	ds_read_b64_tr_b16 v[152:153], v177 offset:0x4000
	ds_read_b64_tr_b16 v[154:155], v177 offset:0x5000
	ds_read_b64_tr_b16 v[156:157], v177 offset:0x6000
	ds_read_b64_tr_b16 v[158:159], v177 offset:0x7000
	ds_read_b64_tr_b16 v[192:193], v177 offset:0x200
	ds_read_b64_tr_b16 v[194:195], v177 offset:0x1200
	ds_read_b64_tr_b16 v[196:197], v177 offset:0x2200
	ds_read_b64_tr_b16 v[198:199], v177 offset:0x3200
	ds_read_b64_tr_b16 v[200:201], v177 offset:0x4200
	ds_read_b64_tr_b16 v[202:203], v177 offset:0x5200
	ds_read_b64_tr_b16 v[204:205], v177 offset:0x6200
	ds_read_b64_tr_b16 v[206:207], v177 offset:0x7200
	s_waitcnt lgkmcnt(8)
	s_nop 0
	v_mfma_f32_32x32x16_bf16 v[112:127], v[144:147], v[128:131], v[112:127]
	v_mfma_f32_32x32x16_bf16 v[112:127], v[148:151], v[132:135], v[112:127]
	v_mfma_f32_32x32x16_bf16 v[112:127], v[152:155], v[136:139], v[112:127]
	v_mfma_f32_32x32x16_bf16 v[112:127], v[156:159], v[140:143], v[112:127]
	ds_read_b64_tr_b16 v[144:145], v177 offset:0x400
	ds_read_b64_tr_b16 v[146:147], v177 offset:0x1400
	ds_read_b64_tr_b16 v[148:149], v177 offset:0x2400
	ds_read_b64_tr_b16 v[150:151], v177 offset:0x3400
	ds_read_b64_tr_b16 v[152:153], v177 offset:0x4400
	ds_read_b64_tr_b16 v[154:155], v177 offset:0x5400
	ds_read_b64_tr_b16 v[156:157], v177 offset:0x6400
	ds_read_b64_tr_b16 v[158:159], v177 offset:0x7400
	s_waitcnt lgkmcnt(8)
	v_mfma_f32_32x32x16_bf16 v[96:111], v[192:195], v[128:131], v[96:111]
	v_mfma_f32_32x32x16_bf16 v[96:111], v[196:199], v[132:135], v[96:111]
	v_mfma_f32_32x32x16_bf16 v[96:111], v[200:203], v[136:139], v[96:111]
	v_mfma_f32_32x32x16_bf16 v[96:111], v[204:207], v[140:143], v[96:111]
	ds_read_b64_tr_b16 v[192:193], v177 offset:0x600
	ds_read_b64_tr_b16 v[194:195], v177 offset:0x1600
	ds_read_b64_tr_b16 v[196:197], v177 offset:0x2600
	ds_read_b64_tr_b16 v[198:199], v177 offset:0x3600
	ds_read_b64_tr_b16 v[200:201], v177 offset:0x4600
	ds_read_b64_tr_b16 v[202:203], v177 offset:0x5600
	ds_read_b64_tr_b16 v[204:205], v177 offset:0x6600
	ds_read_b64_tr_b16 v[206:207], v177 offset:0x7600
	s_waitcnt lgkmcnt(8)
	v_mfma_f32_32x32x16_bf16 v[80:95], v[144:147], v[128:131], v[80:95]
	v_mfma_f32_32x32x16_bf16 v[80:95], v[148:151], v[132:135], v[80:95]
	v_mfma_f32_32x32x16_bf16 v[80:95], v[152:155], v[136:139], v[80:95]
	v_mfma_f32_32x32x16_bf16 v[80:95], v[156:159], v[140:143], v[80:95]
	ds_read_b64_tr_b16 v[144:145], v177 offset:0x800
	ds_read_b64_tr_b16 v[146:147], v177 offset:0x1800
	ds_read_b64_tr_b16 v[148:149], v177 offset:0x2800
	ds_read_b64_tr_b16 v[150:151], v177 offset:0x3800
	ds_read_b64_tr_b16 v[152:153], v177 offset:0x4800
	ds_read_b64_tr_b16 v[154:155], v177 offset:0x5800
	ds_read_b64_tr_b16 v[156:157], v177 offset:0x6800
	ds_read_b64_tr_b16 v[158:159], v177 offset:0x7800
	s_waitcnt lgkmcnt(8)
	v_mfma_f32_32x32x16_bf16 v[64:79], v[192:195], v[128:131], v[64:79]
	v_mfma_f32_32x32x16_bf16 v[64:79], v[196:199], v[132:135], v[64:79]
	v_mfma_f32_32x32x16_bf16 v[64:79], v[200:203], v[136:139], v[64:79]
	v_mfma_f32_32x32x16_bf16 v[64:79], v[204:207], v[140:143], v[64:79]
	ds_read_b64_tr_b16 v[192:193], v177 offset:0xa00
	ds_read_b64_tr_b16 v[194:195], v177 offset:0x1a00
	ds_read_b64_tr_b16 v[196:197], v177 offset:0x2a00
	ds_read_b64_tr_b16 v[198:199], v177 offset:0x3a00
	ds_read_b64_tr_b16 v[200:201], v177 offset:0x4a00
	ds_read_b64_tr_b16 v[202:203], v177 offset:0x5a00
	ds_read_b64_tr_b16 v[204:205], v177 offset:0x6a00
	ds_read_b64_tr_b16 v[206:207], v177 offset:0x7a00
	s_waitcnt lgkmcnt(8)
	v_mfma_f32_32x32x16_bf16 v[48:63], v[144:147], v[128:131], v[48:63]
	v_mfma_f32_32x32x16_bf16 v[48:63], v[148:151], v[132:135], v[48:63]
	v_mfma_f32_32x32x16_bf16 v[48:63], v[152:155], v[136:139], v[48:63]
	v_mfma_f32_32x32x16_bf16 v[48:63], v[156:159], v[140:143], v[48:63]
	ds_read_b64_tr_b16 v[144:145], v177 offset:0xc00
	ds_read_b64_tr_b16 v[146:147], v177 offset:0x1c00
	ds_read_b64_tr_b16 v[148:149], v177 offset:0x2c00
	ds_read_b64_tr_b16 v[150:151], v177 offset:0x3c00
	ds_read_b64_tr_b16 v[152:153], v177 offset:0x4c00
	ds_read_b64_tr_b16 v[154:155], v177 offset:0x5c00
	ds_read_b64_tr_b16 v[156:157], v177 offset:0x6c00
	ds_read_b64_tr_b16 v[158:159], v177 offset:0x7c00
	s_waitcnt lgkmcnt(8)
	v_mfma_f32_32x32x16_bf16 v[32:47], v[192:195], v[128:131], v[32:47]
	v_mfma_f32_32x32x16_bf16 v[32:47], v[196:199], v[132:135], v[32:47]
	v_mfma_f32_32x32x16_bf16 v[32:47], v[200:203], v[136:139], v[32:47]
	v_mfma_f32_32x32x16_bf16 v[32:47], v[204:207], v[140:143], v[32:47]
	ds_read_b64_tr_b16 v[192:193], v177 offset:0xe00
	ds_read_b64_tr_b16 v[194:195], v177 offset:0x1e00
	ds_read_b64_tr_b16 v[196:197], v177 offset:0x2e00
	ds_read_b64_tr_b16 v[198:199], v177 offset:0x3e00
	ds_read_b64_tr_b16 v[200:201], v177 offset:0x4e00
	ds_read_b64_tr_b16 v[202:203], v177 offset:0x5e00
	ds_read_b64_tr_b16 v[204:205], v177 offset:0x6e00
	ds_read_b64_tr_b16 v[206:207], v177 offset:0x7e00
	s_waitcnt lgkmcnt(8)
	v_mfma_f32_32x32x16_bf16 v[16:31], v[144:147], v[128:131], v[16:31]
	v_mfma_f32_32x32x16_bf16 v[16:31], v[148:151], v[132:135], v[16:31]
	v_mfma_f32_32x32x16_bf16 v[16:31], v[152:155], v[136:139], v[16:31]
	v_mfma_f32_32x32x16_bf16 v[16:31], v[156:159], v[140:143], v[16:31]
	s_waitcnt lgkmcnt(0)
	v_mfma_f32_32x32x16_bf16 v[0:15], v[192:195], v[128:131], v[0:15]
	v_mfma_f32_32x32x16_bf16 v[0:15], v[196:199], v[132:135], v[0:15]
	v_mfma_f32_32x32x16_bf16 v[0:15], v[200:203], v[136:139], v[0:15]
	v_mfma_f32_32x32x16_bf16 v[0:15], v[204:207], v[140:143], v[0:15]
	ds_read_b128 v[128:131], v188 offset:0
	ds_read_b128 v[132:135], v188 offset:0x2000
	ds_read_b128 v[136:139], v180 offset:0
	ds_read_b128 v[192:195], v187 offset:0
	ds_read_b128 v[196:199], v187 offset:0x2000
	ds_read_b128 v[200:203], v180 offset:0x400
	s_waitcnt lgkmcnt(3)
	s_nop 0
	v_mfma_f32_32x32x16_bf16 v[144:159], v[128:131], v[136:139], 0
	v_mfma_f32_32x32x16_bf16 v[128:143], v[132:135], v[136:139], 0
	ds_read_b128 v[204:207], v186 offset:0
	ds_read_b128 v[208:211], v186 offset:0x2000
	ds_read_b128 v[212:215], v180 offset:0x800
	s_waitcnt lgkmcnt(3)
	v_mfma_f32_32x32x16_bf16 v[144:159], v[192:195], v[200:203], v[144:159]
	v_mfma_f32_32x32x16_bf16 v[128:143], v[196:199], v[200:203], v[128:143]
	ds_read_b128 v[192:195], v185 offset:0
	ds_read_b128 v[196:199], v185 offset:0x2000
	ds_read_b128 v[200:203], v180 offset:0xc00
	s_waitcnt lgkmcnt(3)
	v_mfma_f32_32x32x16_bf16 v[144:159], v[204:207], v[212:215], v[144:159]
	v_mfma_f32_32x32x16_bf16 v[128:143], v[208:211], v[212:215], v[128:143]
	ds_read_b128 v[204:207], v188 offset:0x80
	ds_read_b128 v[208:211], v188 offset:0x2080
	ds_read_b128 v[212:215], v180 offset:0x1000
	s_waitcnt lgkmcnt(3)
	v_mfma_f32_32x32x16_bf16 v[144:159], v[192:195], v[200:203], v[144:159]
	v_mfma_f32_32x32x16_bf16 v[128:143], v[196:199], v[200:203], v[128:143]
	ds_read_b128 v[192:195], v187 offset:0x80
	ds_read_b128 v[196:199], v187 offset:0x2080
	ds_read_b128 v[200:203], v180 offset:0x1400
	s_waitcnt lgkmcnt(3)
	v_mfma_f32_32x32x16_bf16 v[144:159], v[204:207], v[212:215], v[144:159]
	v_mfma_f32_32x32x16_bf16 v[128:143], v[208:211], v[212:215], v[128:143]
	ds_read_b128 v[204:207], v186 offset:0x80
	ds_read_b128 v[208:211], v186 offset:0x2080
	ds_read_b128 v[212:215], v180 offset:0x1800
	s_waitcnt lgkmcnt(3)
	v_mfma_f32_32x32x16_bf16 v[144:159], v[192:195], v[200:203], v[144:159]
	v_mfma_f32_32x32x16_bf16 v[128:143], v[196:199], v[200:203], v[128:143]
	ds_read_b128 v[192:195], v185 offset:0x80
	ds_read_b128 v[196:199], v185 offset:0x2080
	s_waitcnt lgkmcnt(2)
	v_mfma_f32_32x32x16_bf16 v[144:159], v[204:207], v[212:215], v[144:159]
	v_mfma_f32_32x32x16_bf16 v[128:143], v[208:211], v[212:215], v[128:143]
	s_waitcnt lgkmcnt(0)
	v_mfma_f32_32x32x16_bf16 v[144:159], v[192:195], v[166:169], v[144:159]
	v_mfma_f32_32x32x16_bf16 v[128:143], v[196:199], v[166:169], v[128:143]
	s_bitcmp0_b32 s100, 8
	s_cbranch_scc1 .Lstg_a18
	s_waitcnt vmcnt(0)
	s_waitcnt lgkmcnt(0)
	s_barrier
	s_add_i32 s8, s85, -1
	s_cmp_ge_u32 s8, s75
	s_cbranch_scc1 .Learly_skip_m1_1
	s_add_u32 s6, s76, 0x19f100
	s_addc_u32 s7, s77, 0
	s_mov_b32 m0, s82
	s_nop 0
	global_load_lds_dwordx4 v160, s[6:7]
	s_mov_b32 m0, s84
	s_nop 0
	global_load_lds_dwordx4 v170, s[6:7]
	s_mov_b32 m0, s3
	s_nop 0
	global_load_lds_dwordx4 v162, s[76:77]
	s_add_i32 m0, s69, 0xffffff80
	s_nop 0
	global_load_lds_dwordx4 v162, s[76:77] offset:128
	s_add_i32 m0, s68, 0xffffff00
	s_nop 0
	global_load_lds_dwordx4 v162, s[76:77] offset:256
	s_add_i32 m0, s2, 0xfffffe80
	s_nop 0
	global_load_lds_dwordx4 v162, s[76:77] offset:384
	s_mov_b32 s101, 1
.Learly_skip_m1_1:
.Lstg_a18:
	s_sub_i32 s4, s97, 64
	s_cmp_le_i32 s4, s74
	s_cbranch_scc1 .LBB0_591
	v_add_u32_e32 v172, 64, v189
	v_cmp_gt_i32_e64 s[62:63], 26, v172
	v_cmp_gt_i32_e64 s[64:65], 27, v172
	v_cmp_gt_i32_e64 s[60:61], 25, v172
	s_and_b64 s[62:63], s[64:65], s[62:63]
	v_cmp_gt_i32_e64 s[58:59], 24, v172
	s_and_b64 s[60:61], s[62:63], s[60:61]
	v_cmp_gt_i32_e64 s[56:57], 19, v172
	s_and_b64 s[58:59], s[60:61], s[58:59]
	v_cmp_gt_i32_e64 s[54:55], 18, v172
	s_and_b64 s[56:57], s[58:59], s[56:57]
	v_cmp_gt_i32_e64 s[52:53], 17, v172
	s_and_b64 s[54:55], s[56:57], s[54:55]
	v_cmp_gt_i32_e64 s[50:51], 16, v172
	s_and_b64 s[52:53], s[54:55], s[52:53]
	v_cmp_gt_i32_e64 s[48:49], 11, v172
	s_and_b64 s[50:51], s[52:53], s[50:51]
	v_cmp_gt_i32_e64 s[46:47], 10, v172
	s_and_b64 s[48:49], s[50:51], s[48:49]
	v_cmp_gt_i32_e64 s[44:45], 9, v172
	s_and_b64 s[46:47], s[48:49], s[46:47]
	v_cmp_gt_i32_e64 s[42:43], 8, v172
	s_and_b64 s[44:45], s[46:47], s[44:45]
	v_cmp_gt_i32_e64 s[40:41], 3, v172
	s_and_b64 s[42:43], s[44:45], s[42:43]
	v_cmp_gt_i32_e64 s[38:39], 2, v172
	s_and_b64 s[40:41], s[42:43], s[40:41]
	v_cmp_gt_i32_e64 s[36:37], 1, v172
	s_and_b64 s[38:39], s[40:41], s[38:39]
	v_cmp_gt_i32_e64 s[34:35], 0, v172
	s_and_b64 s[36:37], s[38:39], s[36:37]
	s_and_b64 s[34:35], s[36:37], s[34:35]
	v_cmp_gt_i32_e64 s[30:31], 58, v172
	v_cndmask_b32_e64 v144, v144, v226, s[34:35]
	v_cmp_gt_i32_e64 s[34:35], 59, v172
	v_cmp_gt_i32_e64 s[28:29], 57, v172
	s_and_b64 s[30:31], s[34:35], s[30:31]
	v_cmp_gt_i32_e64 s[26:27], 56, v172
	s_and_b64 s[28:29], s[30:31], s[28:29]
	v_cmp_gt_i32_e64 s[24:25], 51, v172
	s_and_b64 s[26:27], s[28:29], s[26:27]
	v_cmp_gt_i32_e64 s[22:23], 50, v172
	s_and_b64 s[24:25], s[26:27], s[24:25]
	v_cmp_gt_i32_e64 s[20:21], 49, v172
	s_and_b64 s[22:23], s[24:25], s[22:23]
	v_cmp_gt_i32_e64 s[18:19], 48, v172
	s_and_b64 s[20:21], s[22:23], s[20:21]
	v_cmp_gt_i32_e64 s[16:17], 43, v172
	s_and_b64 s[18:19], s[20:21], s[18:19]
	v_cmp_gt_i32_e64 s[14:15], 42, v172
	s_and_b64 s[16:17], s[18:19], s[16:17]
	v_cmp_gt_i32_e64 s[12:13], 41, v172
	s_and_b64 s[14:15], s[16:17], s[14:15]
	v_cmp_gt_i32_e64 s[10:11], 40, v172
	s_and_b64 s[12:13], s[14:15], s[12:13]
	v_cmp_gt_i32_e64 s[8:9], 35, v172
	s_and_b64 s[10:11], s[12:13], s[10:11]
	v_cmp_gt_i32_e64 s[6:7], 34, v172
	s_and_b64 s[8:9], s[10:11], s[8:9]
	v_cmp_gt_i32_e64 s[4:5], 33, v172
	s_and_b64 s[6:7], s[8:9], s[6:7]
	v_cmp_gt_i32_e32 vcc, 32, v172
	s_and_b64 s[4:5], s[6:7], s[4:5]
	s_and_b64 vcc, s[4:5], vcc
	v_cndmask_b32_e64 v159, v159, v226, s[64:65]
	v_cndmask_b32_e64 v158, v158, v226, s[62:63]
	s_mov_b64 s[62:63], 0x100
	v_cndmask_b32_e64 v157, v157, v226, s[60:61]
	v_cndmask_b32_e64 v156, v156, v226, s[58:59]
	v_cndmask_b32_e64 v155, v155, v226, s[56:57]
	v_cndmask_b32_e64 v154, v154, v226, s[54:55]
	v_cndmask_b32_e64 v153, v153, v226, s[52:53]
	v_cndmask_b32_e64 v152, v152, v226, s[50:51]
	v_cndmask_b32_e64 v151, v151, v226, s[48:49]
	v_cndmask_b32_e64 v150, v150, v226, s[46:47]
	v_cndmask_b32_e64 v149, v149, v226, s[44:45]
	v_cndmask_b32_e64 v148, v148, v226, s[42:43]
	v_cndmask_b32_e64 v147, v147, v226, s[40:41]
	v_cndmask_b32_e64 v146, v146, v226, s[38:39]
	v_cndmask_b32_e64 v145, v145, v226, s[36:37]
	v_cndmask_b32_e64 v143, v143, v226, s[34:35]
	v_cndmask_b32_e64 v142, v142, v226, s[30:31]
	v_cndmask_b32_e64 v141, v141, v226, s[28:29]
	v_cndmask_b32_e64 v140, v140, v226, s[26:27]
	v_cndmask_b32_e64 v139, v139, v226, s[24:25]
	v_cndmask_b32_e64 v138, v138, v226, s[22:23]
	v_cndmask_b32_e64 v137, v137, v226, s[20:21]
	v_cndmask_b32_e64 v136, v136, v226, s[18:19]
	v_cndmask_b32_e64 v135, v135, v226, s[16:17]
	v_cndmask_b32_e64 v134, v134, v226, s[14:15]
	v_cndmask_b32_e64 v133, v133, v226, s[12:13]
	v_cndmask_b32_e64 v132, v132, v226, s[10:11]
	v_cndmask_b32_e64 v131, v131, v226, s[8:9]
	v_cndmask_b32_e64 v130, v130, v226, s[6:7]
	v_cndmask_b32_e64 v129, v129, v226, s[4:5]
	v_cndmask_b32_e32 v128, v128, v226, vcc

.LBB0_593:
	s_andn2_b64 vcc, exec, s[6:7]
	s_cbranch_vccnz .LBB0_595
	s_cmp_eq_u32 s101, 1
	s_cbranch_scc1 .LBB0_595
	s_add_u32 s6, s76, 0x19f100
	s_addc_u32 s7, s77, 0
	s_mov_b32 m0, s82
	s_nop 0
	global_load_lds_dwordx4 v160, s[6:7]
	s_mov_b32 m0, s84
	s_nop 0
	global_load_lds_dwordx4 v170, s[6:7]
.LBB0_595:
	v_sub_f32_e32 v144, v190, v172
	v_mul_f32_e32 v144, 0x3e0293ee, v144
	v_exp_f32_e32 v144, v144
	s_nop 0
	v_cndmask_b32_e64 v172, v144, 1.0, s[4:5]
	s_cmp_eq_u32 s101, 1
	s_cbranch_scc1 .Learly_vdone_m1_1
	s_mov_b32 m0, s3
	s_nop 0
	global_load_lds_dwordx4 v162, s[76:77]
	s_add_i32 m0, s69, 0xffffff80
	s_nop 0
	global_load_lds_dwordx4 v162, s[76:77] offset:128
	s_add_i32 m0, s68, 0xffffff00
	s_nop 0
	global_load_lds_dwordx4 v162, s[76:77] offset:256
	s_add_i32 m0, s2, 0xfffffe80
	s_nop 0
	global_load_lds_dwordx4 v162, s[76:77] offset:384
.Learly_vdone_m1_1:
	s_mov_b32 s101, 0
	v_cmp_gt_f32_e32 vcc, 1.0, v172
	s_cbranch_vccz .LBB0_597
	v_pk_mul_f32 v[126:127], v[126:127], v[172:173] op_sel_hi:[1,0]
	v_pk_mul_f32 v[124:125], v[124:125], v[172:173] op_sel_hi:[1,0]
	v_pk_mul_f32 v[122:123], v[122:123], v[172:173] op_sel_hi:[1,0]
	v_pk_mul_f32 v[120:121], v[120:121], v[172:173] op_sel_hi:[1,0]
	v_pk_mul_f32 v[118:119], v[118:119], v[172:173] op_sel_hi:[1,0]
	v_pk_mul_f32 v[116:117], v[116:117], v[172:173] op_sel_hi:[1,0]
	v_pk_mul_f32 v[114:115], v[114:115], v[172:173] op_sel_hi:[1,0]
	v_pk_mul_f32 v[112:113], v[112:113], v[172:173] op_sel_hi:[1,0]
	v_pk_mul_f32 v[110:111], v[110:111], v[172:173] op_sel_hi:[1,0]
	v_pk_mul_f32 v[108:109], v[108:109], v[172:173] op_sel_hi:[1,0]
	v_pk_mul_f32 v[106:107], v[106:107], v[172:173] op_sel_hi:[1,0]
	v_pk_mul_f32 v[104:105], v[104:105], v[172:173] op_sel_hi:[1,0]
	v_pk_mul_f32 v[102:103], v[102:103], v[172:173] op_sel_hi:[1,0]
	v_pk_mul_f32 v[100:101], v[100:101], v[172:173] op_sel_hi:[1,0]
	v_pk_mul_f32 v[98:99], v[98:99], v[172:173] op_sel_hi:[1,0]
	v_pk_mul_f32 v[96:97], v[96:97], v[172:173] op_sel_hi:[1,0]
	v_pk_mul_f32 v[94:95], v[94:95], v[172:173] op_sel_hi:[1,0]
	v_pk_mul_f32 v[92:93], v[92:93], v[172:173] op_sel_hi:[1,0]
	v_pk_mul_f32 v[90:91], v[90:91], v[172:173] op_sel_hi:[1,0]
	v_pk_mul_f32 v[88:89], v[88:89], v[172:173] op_sel_hi:[1,0]
	v_pk_mul_f32 v[86:87], v[86:87], v[172:173] op_sel_hi:[1,0]
	v_pk_mul_f32 v[84:85], v[84:85], v[172:173] op_sel_hi:[1,0]
	v_pk_mul_f32 v[82:83], v[82:83], v[172:173] op_sel_hi:[1,0]
	v_pk_mul_f32 v[80:81], v[80:81], v[172:173] op_sel_hi:[1,0]
	v_pk_mul_f32 v[78:79], v[78:79], v[172:173] op_sel_hi:[1,0]
	v_pk_mul_f32 v[76:77], v[76:77], v[172:173] op_sel_hi:[1,0]
	v_pk_mul_f32 v[74:75], v[74:75], v[172:173] op_sel_hi:[1,0]
	v_pk_mul_f32 v[72:73], v[72:73], v[172:173] op_sel_hi:[1,0]
	v_pk_mul_f32 v[70:71], v[70:71], v[172:173] op_sel_hi:[1,0]
	v_pk_mul_f32 v[68:69], v[68:69], v[172:173] op_sel_hi:[1,0]
	v_pk_mul_f32 v[66:67], v[66:67], v[172:173] op_sel_hi:[1,0]
	v_pk_mul_f32 v[64:65], v[64:65], v[172:173] op_sel_hi:[1,0]
	v_pk_mul_f32 v[62:63], v[62:63], v[172:173] op_sel_hi:[1,0]
	v_pk_mul_f32 v[60:61], v[60:61], v[172:173] op_sel_hi:[1,0]
	v_pk_mul_f32 v[58:59], v[58:59], v[172:173] op_sel_hi:[1,0]
	v_pk_mul_f32 v[56:57], v[56:57], v[172:173] op_sel_hi:[1,0]
	v_pk_mul_f32 v[54:55], v[54:55], v[172:173] op_sel_hi:[1,0]
	v_pk_mul_f32 v[52:53], v[52:53], v[172:173] op_sel_hi:[1,0]
	v_pk_mul_f32 v[50:51], v[50:51], v[172:173] op_sel_hi:[1,0]
	v_pk_mul_f32 v[48:49], v[48:49], v[172:173] op_sel_hi:[1,0]
	v_pk_mul_f32 v[46:47], v[46:47], v[172:173] op_sel_hi:[1,0]
	v_pk_mul_f32 v[44:45], v[44:45], v[172:173] op_sel_hi:[1,0]
	v_pk_mul_f32 v[42:43], v[42:43], v[172:173] op_sel_hi:[1,0]
	v_pk_mul_f32 v[40:41], v[40:41], v[172:173] op_sel_hi:[1,0]
	v_pk_mul_f32 v[38:39], v[38:39], v[172:173] op_sel_hi:[1,0]
	v_pk_mul_f32 v[36:37], v[36:37], v[172:173] op_sel_hi:[1,0]
	v_pk_mul_f32 v[34:35], v[34:35], v[172:173] op_sel_hi:[1,0]
	v_pk_mul_f32 v[32:33], v[32:33], v[172:173] op_sel_hi:[1,0]
	v_pk_mul_f32 v[30:31], v[30:31], v[172:173] op_sel_hi:[1,0]
	v_pk_mul_f32 v[28:29], v[28:29], v[172:173] op_sel_hi:[1,0]
	v_pk_mul_f32 v[26:27], v[26:27], v[172:173] op_sel_hi:[1,0]
	v_pk_mul_f32 v[24:25], v[24:25], v[172:173] op_sel_hi:[1,0]
	v_pk_mul_f32 v[22:23], v[22:23], v[172:173] op_sel_hi:[1,0]
	v_pk_mul_f32 v[20:21], v[20:21], v[172:173] op_sel_hi:[1,0]
	v_pk_mul_f32 v[18:19], v[18:19], v[172:173] op_sel_hi:[1,0]
	v_pk_mul_f32 v[16:17], v[16:17], v[172:173] op_sel_hi:[1,0]
	v_pk_mul_f32 v[14:15], v[14:15], v[172:173] op_sel_hi:[1,0]
	v_pk_mul_f32 v[12:13], v[12:13], v[172:173] op_sel_hi:[1,0]
	v_pk_mul_f32 v[10:11], v[10:11], v[172:173] op_sel_hi:[1,0]
	v_pk_mul_f32 v[8:9], v[8:9], v[172:173] op_sel_hi:[1,0]
	v_pk_mul_f32 v[6:7], v[6:7], v[172:173] op_sel_hi:[1,0]
	v_pk_mul_f32 v[4:5], v[4:5], v[172:173] op_sel_hi:[1,0]
	v_pk_mul_f32 v[2:3], v[2:3], v[172:173] op_sel_hi:[1,0]
	v_pk_mul_f32 v[0:1], v[0:1], v[172:173] op_sel_hi:[1,0]
.LBB0_597:
	ds_read_b64_tr_b16 v[144:145], v177 offset:0x8000
	ds_read_b64_tr_b16 v[146:147], v177 offset:0x9000
	ds_read_b64_tr_b16 v[148:149], v177 offset:0xa000
	ds_read_b64_tr_b16 v[150:151], v177 offset:0xb000
	ds_read_b64_tr_b16 v[152:153], v177 offset:0xc000
	ds_read_b64_tr_b16 v[154:155], v177 offset:0xd000
	ds_read_b64_tr_b16 v[156:157], v177 offset:0xe000
	ds_read_b64_tr_b16 v[158:159], v177 offset:0xf000
	ds_read_b64_tr_b16 v[194:195], v177 offset:0x8200
	ds_read_b64_tr_b16 v[196:197], v177 offset:0x9200
	ds_read_b64_tr_b16 v[198:199], v177 offset:0xa200
	ds_read_b64_tr_b16 v[200:201], v177 offset:0xb200
	ds_read_b64_tr_b16 v[202:203], v177 offset:0xc200
	ds_read_b64_tr_b16 v[204:205], v177 offset:0xd200
	ds_read_b64_tr_b16 v[206:207], v177 offset:0xe200
	ds_read_b64_tr_b16 v[208:209], v177 offset:0xf200
	s_waitcnt lgkmcnt(8)
	s_nop 0
	v_mfma_f32_32x32x16_bf16 v[112:127], v[144:147], v[128:131], v[112:127]
	v_mfma_f32_32x32x16_bf16 v[112:127], v[148:151], v[132:135], v[112:127]
	v_mfma_f32_32x32x16_bf16 v[112:127], v[152:155], v[136:139], v[112:127]
	v_mfma_f32_32x32x16_bf16 v[112:127], v[156:159], v[140:143], v[112:127]
	ds_read_b64_tr_b16 v[144:145], v177 offset:0x8400
	ds_read_b64_tr_b16 v[146:147], v177 offset:0x9400
	ds_read_b64_tr_b16 v[148:149], v177 offset:0xa400
	ds_read_b64_tr_b16 v[150:151], v177 offset:0xb400
	ds_read_b64_tr_b16 v[152:153], v177 offset:0xc400
	ds_read_b64_tr_b16 v[154:155], v177 offset:0xd400
	ds_read_b64_tr_b16 v[156:157], v177 offset:0xe400
	ds_read_b64_tr_b16 v[158:159], v177 offset:0xf400
	s_waitcnt lgkmcnt(8)
	v_mfma_f32_32x32x16_bf16 v[96:111], v[194:197], v[128:131], v[96:111]
	v_mfma_f32_32x32x16_bf16 v[96:111], v[198:201], v[132:135], v[96:111]
	v_mfma_f32_32x32x16_bf16 v[96:111], v[202:205], v[136:139], v[96:111]
	v_mfma_f32_32x32x16_bf16 v[96:111], v[206:209], v[140:143], v[96:111]
	ds_read_b64_tr_b16 v[194:195], v177 offset:0x8600
	ds_read_b64_tr_b16 v[196:197], v177 offset:0x9600
	ds_read_b64_tr_b16 v[198:199], v177 offset:0xa600
	ds_read_b64_tr_b16 v[200:201], v177 offset:0xb600
	ds_read_b64_tr_b16 v[202:203], v177 offset:0xc600
	ds_read_b64_tr_b16 v[204:205], v177 offset:0xd600
	ds_read_b64_tr_b16 v[206:207], v177 offset:0xe600
	ds_read_b64_tr_b16 v[208:209], v177 offset:0xf600
	s_waitcnt lgkmcnt(8)
	v_mfma_f32_32x32x16_bf16 v[80:95], v[144:147], v[128:131], v[80:95]
	v_mfma_f32_32x32x16_bf16 v[80:95], v[148:151], v[132:135], v[80:95]
	v_mfma_f32_32x32x16_bf16 v[80:95], v[152:155], v[136:139], v[80:95]
	v_mfma_f32_32x32x16_bf16 v[80:95], v[156:159], v[140:143], v[80:95]
	ds_read_b64_tr_b16 v[144:145], v177 offset:0x8800
	ds_read_b64_tr_b16 v[146:147], v177 offset:0x9800
	ds_read_b64_tr_b16 v[148:149], v177 offset:0xa800
	ds_read_b64_tr_b16 v[150:151], v177 offset:0xb800
	ds_read_b64_tr_b16 v[152:153], v177 offset:0xc800
	ds_read_b64_tr_b16 v[154:155], v177 offset:0xd800
	ds_read_b64_tr_b16 v[156:157], v177 offset:0xe800
	ds_read_b64_tr_b16 v[158:159], v177 offset:0xf800
	s_waitcnt lgkmcnt(8)
	v_mfma_f32_32x32x16_bf16 v[64:79], v[194:197], v[128:131], v[64:79]
	v_mfma_f32_32x32x16_bf16 v[64:79], v[198:201], v[132:135], v[64:79]
	v_mfma_f32_32x32x16_bf16 v[64:79], v[202:205], v[136:139], v[64:79]
	v_mfma_f32_32x32x16_bf16 v[64:79], v[206:209], v[140:143], v[64:79]
	ds_read_b64_tr_b16 v[194:195], v177 offset:0x8a00
	ds_read_b64_tr_b16 v[196:197], v177 offset:0x9a00
	ds_read_b64_tr_b16 v[198:199], v177 offset:0xaa00
	ds_read_b64_tr_b16 v[200:201], v177 offset:0xba00
	ds_read_b64_tr_b16 v[202:203], v177 offset:0xca00
	ds_read_b64_tr_b16 v[204:205], v177 offset:0xda00
	ds_read_b64_tr_b16 v[206:207], v177 offset:0xea00
	ds_read_b64_tr_b16 v[208:209], v177 offset:0xfa00
	s_waitcnt lgkmcnt(8)
	v_mfma_f32_32x32x16_bf16 v[48:63], v[144:147], v[128:131], v[48:63]
	v_mfma_f32_32x32x16_bf16 v[48:63], v[148:151], v[132:135], v[48:63]
	v_mfma_f32_32x32x16_bf16 v[48:63], v[152:155], v[136:139], v[48:63]
	v_mfma_f32_32x32x16_bf16 v[48:63], v[156:159], v[140:143], v[48:63]
	ds_read_b64_tr_b16 v[144:145], v177 offset:0x8c00
	ds_read_b64_tr_b16 v[146:147], v177 offset:0x9c00
	ds_read_b64_tr_b16 v[148:149], v177 offset:0xac00
	ds_read_b64_tr_b16 v[150:151], v177 offset:0xbc00
	ds_read_b64_tr_b16 v[152:153], v177 offset:0xcc00
	ds_read_b64_tr_b16 v[154:155], v177 offset:0xdc00
	ds_read_b64_tr_b16 v[156:157], v177 offset:0xec00
	ds_read_b64_tr_b16 v[158:159], v177 offset:0xfc00
	s_waitcnt lgkmcnt(8)
	v_mfma_f32_32x32x16_bf16 v[32:47], v[194:197], v[128:131], v[32:47]
	v_mfma_f32_32x32x16_bf16 v[32:47], v[198:201], v[132:135], v[32:47]
	v_mfma_f32_32x32x16_bf16 v[32:47], v[202:205], v[136:139], v[32:47]
	v_mfma_f32_32x32x16_bf16 v[32:47], v[206:209], v[140:143], v[32:47]
	ds_read_b64_tr_b16 v[194:195], v177 offset:0x8e00
	ds_read_b64_tr_b16 v[196:197], v177 offset:0x9e00
	ds_read_b64_tr_b16 v[198:199], v177 offset:0xae00
	ds_read_b64_tr_b16 v[200:201], v177 offset:0xbe00
	ds_read_b64_tr_b16 v[202:203], v177 offset:0xce00
	ds_read_b64_tr_b16 v[204:205], v177 offset:0xde00
	ds_read_b64_tr_b16 v[206:207], v177 offset:0xee00
	ds_read_b64_tr_b16 v[208:209], v177 offset:0xfe00
	s_waitcnt lgkmcnt(8)
	v_mfma_f32_32x32x16_bf16 v[16:31], v[144:147], v[128:131], v[16:31]
	v_mfma_f32_32x32x16_bf16 v[16:31], v[148:151], v[132:135], v[16:31]
	v_mfma_f32_32x32x16_bf16 v[16:31], v[152:155], v[136:139], v[16:31]
	v_mfma_f32_32x32x16_bf16 v[16:31], v[156:159], v[140:143], v[16:31]
	s_waitcnt lgkmcnt(0)
	v_mfma_f32_32x32x16_bf16 v[0:15], v[194:197], v[128:131], v[0:15]
	v_mfma_f32_32x32x16_bf16 v[0:15], v[198:201], v[132:135], v[0:15]
	v_mfma_f32_32x32x16_bf16 v[0:15], v[202:205], v[136:139], v[0:15]
	v_mfma_f32_32x32x16_bf16 v[0:15], v[206:209], v[140:143], v[0:15]
	ds_read_b128 v[128:131], v181 offset:0
	ds_read_b128 v[132:135], v181 offset:0x2000
	ds_read_b128 v[136:139], v180 offset:0
	ds_read_b128 v[194:197], v182 offset:0
	ds_read_b128 v[198:201], v182 offset:0x2000
	ds_read_b128 v[202:205], v180 offset:0x400
	s_waitcnt lgkmcnt(3)
	s_nop 0
	v_mfma_f32_32x32x16_bf16 v[144:159], v[128:131], v[136:139], 0
	v_mfma_f32_32x32x16_bf16 v[128:143], v[132:135], v[136:139], 0
	ds_read_b128 v[206:209], v183 offset:0
	ds_read_b128 v[210:213], v183 offset:0x2000
	ds_read_b128 v[214:217], v180 offset:0x800
	s_waitcnt lgkmcnt(3)
	v_mfma_f32_32x32x16_bf16 v[144:159], v[194:197], v[202:205], v[144:159]
	v_mfma_f32_32x32x16_bf16 v[128:143], v[198:201], v[202:205], v[128:143]
	ds_read_b128 v[194:197], v184 offset:0
	ds_read_b128 v[198:201], v184 offset:0x2000
	ds_read_b128 v[202:205], v180 offset:0xc00
	s_waitcnt lgkmcnt(3)
	v_mfma_f32_32x32x16_bf16 v[144:159], v[206:209], v[214:217], v[144:159]
	v_mfma_f32_32x32x16_bf16 v[128:143], v[210:213], v[214:217], v[128:143]
	ds_read_b128 v[206:209], v181 offset:0x80
	ds_read_b128 v[210:213], v181 offset:0x2080
	ds_read_b128 v[214:217], v180 offset:0x1000
	s_waitcnt lgkmcnt(3)
	v_mfma_f32_32x32x16_bf16 v[144:159], v[194:197], v[202:205], v[144:159]
	v_mfma_f32_32x32x16_bf16 v[128:143], v[198:201], v[202:205], v[128:143]
	ds_read_b128 v[194:197], v182 offset:0x80
	ds_read_b128 v[198:201], v182 offset:0x2080
	ds_read_b128 v[202:205], v180 offset:0x1400
	s_waitcnt lgkmcnt(3)
	v_mfma_f32_32x32x16_bf16 v[144:159], v[206:209], v[214:217], v[144:159]
	v_mfma_f32_32x32x16_bf16 v[128:143], v[210:213], v[214:217], v[128:143]
	ds_read_b128 v[206:209], v183 offset:0x80
	ds_read_b128 v[210:213], v183 offset:0x2080
	ds_read_b128 v[214:217], v180 offset:0x1800
	s_waitcnt lgkmcnt(3)
	v_mfma_f32_32x32x16_bf16 v[144:159], v[194:197], v[202:205], v[144:159]
	v_mfma_f32_32x32x16_bf16 v[128:143], v[198:201], v[202:205], v[128:143]
	ds_read_b128 v[194:197], v184 offset:0x80
	ds_read_b128 v[198:201], v184 offset:0x2080
	s_waitcnt lgkmcnt(2)
	v_mfma_f32_32x32x16_bf16 v[144:159], v[206:209], v[214:217], v[144:159]
	v_mfma_f32_32x32x16_bf16 v[128:143], v[210:213], v[214:217], v[128:143]
	s_waitcnt lgkmcnt(0)
	v_mfma_f32_32x32x16_bf16 v[144:159], v[194:197], v[166:169], v[144:159]
	v_mfma_f32_32x32x16_bf16 v[128:143], v[198:201], v[166:169], v[128:143]
	s_bitcmp0_b32 s100, 8
	s_cbranch_scc1 .Lstg_a19
	s_waitcnt vmcnt(0)
	s_waitcnt lgkmcnt(0)
	s_barrier
	s_cmp_lt_u32 s85, s75
	s_cbranch_scc0 .Learly_skip_m1_2
	s_add_u32 s6, s76, 0x33f100
	s_addc_u32 s7, s77, 0
	s_mov_b32 m0, s78
	s_nop 0
	global_load_lds_dwordx4 v160, s[6:7]
	s_mov_b32 m0, s93
	s_nop 0
	global_load_lds_dwordx4 v170, s[6:7]
	s_add_u32 s6, s76, 0x1a0000
	s_addc_u32 s7, s77, 0
	s_mov_b32 m0, s90
	s_nop 0
	global_load_lds_dwordx4 v162, s[6:7]
	s_add_i32 m0, s91, 0xffffff80
	s_nop 0
	global_load_lds_dwordx4 v162, s[6:7] offset:128
	s_add_i32 m0, s88, 0xffffff00
	s_nop 0
	global_load_lds_dwordx4 v162, s[6:7] offset:256
	s_add_i32 m0, s89, 0xfffffe80
	s_nop 0
	global_load_lds_dwordx4 v162, s[6:7] offset:384
	s_mov_b32 s101, 1
.Learly_skip_m1_2:
.Lstg_a19:
	s_cmp_le_i32 s97, s74
	s_cbranch_scc1 .LBB0_599
	v_cmp_gt_i32_e64 s[62:63], 26, v189
	v_cmp_gt_i32_e64 s[64:65], 27, v189
	v_cmp_gt_i32_e64 s[60:61], 25, v189
	s_and_b64 s[62:63], s[64:65], s[62:63]
	v_cmp_gt_i32_e64 s[58:59], 24, v189
	s_and_b64 s[60:61], s[62:63], s[60:61]
	v_cmp_gt_i32_e64 s[56:57], 19, v189
	s_and_b64 s[58:59], s[60:61], s[58:59]
	v_cmp_gt_i32_e64 s[54:55], 18, v189
	s_and_b64 s[56:57], s[58:59], s[56:57]
	v_cmp_gt_i32_e64 s[52:53], 17, v189
	s_and_b64 s[54:55], s[56:57], s[54:55]
	v_cmp_gt_i32_e64 s[50:51], 16, v189
	s_and_b64 s[52:53], s[54:55], s[52:53]
	v_cmp_gt_i32_e64 s[48:49], 11, v189
	s_and_b64 s[50:51], s[52:53], s[50:51]
	v_cmp_gt_i32_e64 s[46:47], 10, v189
	s_and_b64 s[48:49], s[50:51], s[48:49]
	v_cmp_gt_i32_e64 s[44:45], 9, v189
	s_and_b64 s[46:47], s[48:49], s[46:47]
	v_cmp_gt_i32_e64 s[42:43], 8, v189
	s_and_b64 s[44:45], s[46:47], s[44:45]
	v_cmp_gt_i32_e64 s[40:41], 3, v189
	s_and_b64 s[42:43], s[44:45], s[42:43]
	v_cmp_gt_i32_e64 s[38:39], 2, v189
	s_and_b64 s[40:41], s[42:43], s[40:41]
	v_cmp_gt_i32_e64 s[36:37], 1, v189
	s_and_b64 s[38:39], s[40:41], s[38:39]
	v_cmp_gt_i32_e64 s[34:35], 0, v189
	s_and_b64 s[36:37], s[38:39], s[36:37]
	s_and_b64 s[34:35], s[36:37], s[34:35]
	v_cmp_gt_i32_e64 s[30:31], 58, v189
	v_cndmask_b32_e64 v144, v144, v226, s[34:35]
	v_cmp_gt_i32_e64 s[34:35], 59, v189
	v_cmp_gt_i32_e64 s[28:29], 57, v189
	s_and_b64 s[30:31], s[34:35], s[30:31]
	v_cmp_gt_i32_e64 s[26:27], 56, v189
	s_and_b64 s[28:29], s[30:31], s[28:29]
	v_cmp_gt_i32_e64 s[24:25], 51, v189
	s_and_b64 s[26:27], s[28:29], s[26:27]
	v_cmp_gt_i32_e64 s[22:23], 50, v189
	s_and_b64 s[24:25], s[26:27], s[24:25]
	v_cmp_gt_i32_e64 s[20:21], 49, v189
	s_and_b64 s[22:23], s[24:25], s[22:23]
	v_cmp_gt_i32_e64 s[18:19], 48, v189
	s_and_b64 s[20:21], s[22:23], s[20:21]
	v_cmp_gt_i32_e64 s[16:17], 43, v189
	s_and_b64 s[18:19], s[20:21], s[18:19]
	v_cmp_gt_i32_e64 s[14:15], 42, v189
	s_and_b64 s[16:17], s[18:19], s[16:17]
	v_cmp_gt_i32_e64 s[12:13], 41, v189
	s_and_b64 s[14:15], s[16:17], s[14:15]
	v_cmp_gt_i32_e64 s[10:11], 40, v189
	s_and_b64 s[12:13], s[14:15], s[12:13]
	v_cmp_gt_i32_e64 s[8:9], 35, v189
	s_and_b64 s[10:11], s[12:13], s[10:11]
	v_cmp_gt_i32_e64 s[6:7], 34, v189
	s_and_b64 s[8:9], s[10:11], s[8:9]
	v_cmp_gt_i32_e64 s[4:5], 33, v189
	s_and_b64 s[6:7], s[8:9], s[6:7]
	v_cmp_gt_i32_e32 vcc, 32, v189
	s_and_b64 s[4:5], s[6:7], s[4:5]
	s_and_b64 vcc, s[4:5], vcc
	v_cndmask_b32_e64 v159, v159, v226, s[64:65]
	v_cndmask_b32_e64 v158, v158, v226, s[62:63]
	s_mov_b64 s[62:63], 0x100
	v_cndmask_b32_e64 v157, v157, v226, s[60:61]
	v_cndmask_b32_e64 v156, v156, v226, s[58:59]
	v_cndmask_b32_e64 v155, v155, v226, s[56:57]
	v_cndmask_b32_e64 v154, v154, v226, s[54:55]
	v_cndmask_b32_e64 v153, v153, v226, s[52:53]
	v_cndmask_b32_e64 v152, v152, v226, s[50:51]
	v_cndmask_b32_e64 v151, v151, v226, s[48:49]
	v_cndmask_b32_e64 v150, v150, v226, s[46:47]
	v_cndmask_b32_e64 v149, v149, v226, s[44:45]
	v_cndmask_b32_e64 v148, v148, v226, s[42:43]
	v_cndmask_b32_e64 v147, v147, v226, s[40:41]
	v_cndmask_b32_e64 v146, v146, v226, s[38:39]
	v_cndmask_b32_e64 v145, v145, v226, s[36:37]
	v_cndmask_b32_e64 v143, v143, v226, s[34:35]
	v_cndmask_b32_e64 v142, v142, v226, s[30:31]
	v_cndmask_b32_e64 v141, v141, v226, s[28:29]
	v_cndmask_b32_e64 v140, v140, v226, s[26:27]
	v_cndmask_b32_e64 v139, v139, v226, s[24:25]
	v_cndmask_b32_e64 v138, v138, v226, s[22:23]
	v_cndmask_b32_e64 v137, v137, v226, s[20:21]
	v_cndmask_b32_e64 v136, v136, v226, s[18:19]
	v_cndmask_b32_e64 v135, v135, v226, s[16:17]
	v_cndmask_b32_e64 v134, v134, v226, s[14:15]
	v_cndmask_b32_e64 v133, v133, v226, s[12:13]
	v_cndmask_b32_e64 v132, v132, v226, s[10:11]
	v_cndmask_b32_e64 v131, v131, v226, s[8:9]
	v_cndmask_b32_e64 v130, v130, v226, s[6:7]
	v_cndmask_b32_e64 v129, v129, v226, s[4:5]
	v_cndmask_b32_e32 v128, v128, v226, vcc

.LBB0_602:
	s_andn2_b64 vcc, exec, s[6:7]
	s_cbranch_vccnz .LBB0_604
	s_cmp_eq_u32 s101, 1
	s_cbranch_scc1 .LBB0_604
	s_add_u32 s6, s76, 0x33f100
	s_addc_u32 s7, s77, 0
	s_mov_b32 m0, s78
	s_nop 0
	global_load_lds_dwordx4 v160, s[6:7]
	s_mov_b32 m0, s93
	s_nop 0
	global_load_lds_dwordx4 v170, s[6:7]

.LBB0_606:
	s_andn2_b64 vcc, exec, s[6:7]
	s_cbranch_vccnz .LBB0_608
	s_cmp_eq_u32 s101, 1
	s_cbranch_scc1 .LBB0_608
	s_add_u32 s6, s76, 0x1a0000
	s_addc_u32 s7, s77, 0
	s_mov_b32 m0, s90
	s_nop 0
	global_load_lds_dwordx4 v162, s[6:7]
	s_add_i32 m0, s91, 0xffffff80
	s_nop 0
	global_load_lds_dwordx4 v162, s[6:7] offset:128
	s_add_i32 m0, s88, 0xffffff00
	s_nop 0
	global_load_lds_dwordx4 v162, s[6:7] offset:256
	s_add_i32 m0, s89, 0xfffffe80
	s_nop 0
	global_load_lds_dwordx4 v162, s[6:7] offset:384
.LBB0_608:
	s_mov_b32 s101, 0
	v_sub_f32_e32 v144, v193, v198
	v_mul_f32_e32 v144, 0x3e0293ee, v144
	v_exp_f32_e32 v144, v144
	s_nop 0
	v_cndmask_b32_e64 v144, v144, 1.0, s[4:5]
	v_cmp_gt_f32_e32 vcc, 1.0, v144
	s_cbranch_vccz .LBB0_610
	v_pk_mul_f32 v[126:127], v[126:127], v[144:145] op_sel_hi:[1,0]
	v_pk_mul_f32 v[124:125], v[124:125], v[144:145] op_sel_hi:[1,0]
	v_pk_mul_f32 v[122:123], v[122:123], v[144:145] op_sel_hi:[1,0]
	v_pk_mul_f32 v[120:121], v[120:121], v[144:145] op_sel_hi:[1,0]
	v_pk_mul_f32 v[118:119], v[118:119], v[144:145] op_sel_hi:[1,0]
	v_pk_mul_f32 v[116:117], v[116:117], v[144:145] op_sel_hi:[1,0]
	v_pk_mul_f32 v[114:115], v[114:115], v[144:145] op_sel_hi:[1,0]
	v_pk_mul_f32 v[112:113], v[112:113], v[144:145] op_sel_hi:[1,0]
	v_pk_mul_f32 v[110:111], v[110:111], v[144:145] op_sel_hi:[1,0]
	v_pk_mul_f32 v[108:109], v[108:109], v[144:145] op_sel_hi:[1,0]
	v_pk_mul_f32 v[106:107], v[106:107], v[144:145] op_sel_hi:[1,0]
	v_pk_mul_f32 v[104:105], v[104:105], v[144:145] op_sel_hi:[1,0]
	v_pk_mul_f32 v[102:103], v[102:103], v[144:145] op_sel_hi:[1,0]
	v_pk_mul_f32 v[100:101], v[100:101], v[144:145] op_sel_hi:[1,0]
	v_pk_mul_f32 v[98:99], v[98:99], v[144:145] op_sel_hi:[1,0]
	v_pk_mul_f32 v[96:97], v[96:97], v[144:145] op_sel_hi:[1,0]
	v_pk_mul_f32 v[94:95], v[94:95], v[144:145] op_sel_hi:[1,0]
	v_pk_mul_f32 v[92:93], v[92:93], v[144:145] op_sel_hi:[1,0]
	v_pk_mul_f32 v[90:91], v[90:91], v[144:145] op_sel_hi:[1,0]
	v_pk_mul_f32 v[88:89], v[88:89], v[144:145] op_sel_hi:[1,0]
	v_pk_mul_f32 v[86:87], v[86:87], v[144:145] op_sel_hi:[1,0]
	v_pk_mul_f32 v[84:85], v[84:85], v[144:145] op_sel_hi:[1,0]
	v_pk_mul_f32 v[82:83], v[82:83], v[144:145] op_sel_hi:[1,0]
	v_pk_mul_f32 v[80:81], v[80:81], v[144:145] op_sel_hi:[1,0]
	v_pk_mul_f32 v[78:79], v[78:79], v[144:145] op_sel_hi:[1,0]
	v_pk_mul_f32 v[76:77], v[76:77], v[144:145] op_sel_hi:[1,0]
	v_pk_mul_f32 v[74:75], v[74:75], v[144:145] op_sel_hi:[1,0]
	v_pk_mul_f32 v[72:73], v[72:73], v[144:145] op_sel_hi:[1,0]
	v_pk_mul_f32 v[70:71], v[70:71], v[144:145] op_sel_hi:[1,0]
	v_pk_mul_f32 v[68:69], v[68:69], v[144:145] op_sel_hi:[1,0]
	v_pk_mul_f32 v[66:67], v[66:67], v[144:145] op_sel_hi:[1,0]
	v_pk_mul_f32 v[64:65], v[64:65], v[144:145] op_sel_hi:[1,0]
	v_pk_mul_f32 v[62:63], v[62:63], v[144:145] op_sel_hi:[1,0]
	v_pk_mul_f32 v[60:61], v[60:61], v[144:145] op_sel_hi:[1,0]
	v_pk_mul_f32 v[58:59], v[58:59], v[144:145] op_sel_hi:[1,0]
	v_pk_mul_f32 v[56:57], v[56:57], v[144:145] op_sel_hi:[1,0]
	v_pk_mul_f32 v[54:55], v[54:55], v[144:145] op_sel_hi:[1,0]
	v_pk_mul_f32 v[52:53], v[52:53], v[144:145] op_sel_hi:[1,0]
	v_pk_mul_f32 v[50:51], v[50:51], v[144:145] op_sel_hi:[1,0]
	v_pk_mul_f32 v[48:49], v[48:49], v[144:145] op_sel_hi:[1,0]
	v_pk_mul_f32 v[46:47], v[46:47], v[144:145] op_sel_hi:[1,0]
	v_pk_mul_f32 v[44:45], v[44:45], v[144:145] op_sel_hi:[1,0]
	v_pk_mul_f32 v[42:43], v[42:43], v[144:145] op_sel_hi:[1,0]
	v_pk_mul_f32 v[40:41], v[40:41], v[144:145] op_sel_hi:[1,0]
	v_pk_mul_f32 v[38:39], v[38:39], v[144:145] op_sel_hi:[1,0]
	v_pk_mul_f32 v[36:37], v[36:37], v[144:145] op_sel_hi:[1,0]
	v_pk_mul_f32 v[34:35], v[34:35], v[144:145] op_sel_hi:[1,0]
	v_pk_mul_f32 v[32:33], v[32:33], v[144:145] op_sel_hi:[1,0]
	v_pk_mul_f32 v[30:31], v[30:31], v[144:145] op_sel_hi:[1,0]
	v_pk_mul_f32 v[28:29], v[28:29], v[144:145] op_sel_hi:[1,0]
	v_pk_mul_f32 v[26:27], v[26:27], v[144:145] op_sel_hi:[1,0]
	v_pk_mul_f32 v[24:25], v[24:25], v[144:145] op_sel_hi:[1,0]
	v_pk_mul_f32 v[22:23], v[22:23], v[144:145] op_sel_hi:[1,0]
	v_pk_mul_f32 v[20:21], v[20:21], v[144:145] op_sel_hi:[1,0]
	v_pk_mul_f32 v[18:19], v[18:19], v[144:145] op_sel_hi:[1,0]
	v_pk_mul_f32 v[16:17], v[16:17], v[144:145] op_sel_hi:[1,0]
	v_pk_mul_f32 v[14:15], v[14:15], v[144:145] op_sel_hi:[1,0]
	v_pk_mul_f32 v[12:13], v[12:13], v[144:145] op_sel_hi:[1,0]
	v_pk_mul_f32 v[10:11], v[10:11], v[144:145] op_sel_hi:[1,0]
	v_pk_mul_f32 v[8:9], v[8:9], v[144:145] op_sel_hi:[1,0]
	v_pk_mul_f32 v[6:7], v[6:7], v[144:145] op_sel_hi:[1,0]
	v_pk_mul_f32 v[4:5], v[4:5], v[144:145] op_sel_hi:[1,0]
	v_pk_mul_f32 v[2:3], v[2:3], v[144:145] op_sel_hi:[1,0]
	v_pk_mul_f32 v[0:1], v[0:1], v[144:145] op_sel_hi:[1,0]
